# stacked issue-slot trims: SwiGLU epilogue re-emitted with shared reciprocals (phase I), attention tile loops (one V address register + offsets, float key index, max tree and sum chain without canonica
# speedup vs baseline: 1.0389x; 1.0008x over previous
.LBB0_258:
	v_lshlrev_b32_e32 v10, 2, v174
	v_xor_b32_e32 v179, 0x80, v10
	v_max_f32_e32 v10, v0, v0
	v_max_f32_e32 v11, v21, v21
	v_max_f32_e32 v10, v11, v10
	v_max3_f32 v10, v10, v1, v18
	v_max3_f32 v10, v10, v19, v4
	v_max3_f32 v10, v10, v5, v6
	v_max3_f32 v10, v10, v7, v8
	v_max3_f32 v10, v10, v9, v2
	v_max3_f32 v10, v10, v3, v16
	v_max3_f32 v10, v10, v17, v37
	ds_bpermute_b32 v11, v179, v10
	v_mul_u32_u24_e32 v32, 0x410, v34
	s_add_i32 s31, 0, 0x12000
	v_lshl_add_u32 v12, s52, 1, v35
	v_add3_u32 v152, s31, v32, v12
	s_waitcnt lgkmcnt(0)
	v_max_f32_e32 v11, v11, v11
	v_max_f32_e32 v178, v10, v11
	v_sub_f32_e32 v0, v0, v178
	v_exp_f32_e32 v46, v0
	v_sub_f32_e32 v0, v1, v178
	v_exp_f32_e32 v47, v0
	v_sub_f32_e32 v0, v18, v178
	v_exp_f32_e32 v146, v0
	v_sub_f32_e32 v0, v19, v178
	v_exp_f32_e32 v147, v0
	v_sub_f32_e32 v0, v4, v178
	v_exp_f32_e32 v148, v0
	v_sub_f32_e32 v0, v5, v178
	v_exp_f32_e32 v149, v0
	v_sub_f32_e32 v0, v6, v178
	v_exp_f32_e32 v150, v0
	v_sub_f32_e32 v0, v7, v178
	ds_read_b128 v[4:7], v152
	ds_read_b128 v[38:41], v152 offset:32
	v_sub_f32_e32 v10, v21, v178
	v_exp_f32_e32 v33, v10
	v_exp_f32_e32 v151, v0
	v_sub_f32_e32 v0, v9, v178
	v_cvt_pk_bf16_f32 v21, v149, v150
	v_cvt_pk_bf16_f32 v20, v147, v148
	v_cvt_pk_bf16_f32 v19, v47, v146
	v_cvt_pk_bf16_f32 v18, v33, v46
	v_sub_f32_e32 v42, v8, v178
	v_exp_f32_e32 v153, v0
	v_sub_f32_e32 v43, v2, v178
	v_sub_f32_e32 v26, v3, v178
	ds_read_b128 v[22:25], v152 offset:33280
	s_waitcnt lgkmcnt(2)
	v_mfma_f32_32x32x16_bf16 v[0:15], v[4:7], v[18:21], 0
	v_sub_f32_e32 v44, v16, v178
	v_sub_f32_e32 v16, v17, v178
	v_exp_f32_e32 v155, v16
	v_sub_f32_e32 v16, v37, v178
	v_exp_f32_e32 v154, v26
	v_exp_f32_e32 v37, v16
	v_exp_f32_e32 v156, v44
	v_exp_f32_e32 v157, v43
	v_exp_f32_e32 v158, v42
	v_add_f32_e32 v33, 0, v33
	v_add_f32_e32 v33, v46, v33
	v_add_f32_e32 v33, v47, v33
	v_cvt_pk_bf16_f32 v45, v155, v37
	v_cvt_pk_bf16_f32 v44, v154, v156
	v_cvt_pk_bf16_f32 v43, v153, v157
	v_cvt_pk_bf16_f32 v42, v151, v158
	v_add_f32_e32 v33, v146, v33
	v_add_f32_e32 v33, v147, v33
	s_waitcnt lgkmcnt(1)
	v_mfma_f32_32x32x16_bf16 v[0:15], v[38:41], v[42:45], v[0:15]
	ds_read_b128 v[38:41], v152 offset:33312
	v_add_f32_e32 v33, v148, v33
	v_add_f32_e32 v33, v149, v33
	v_add_f32_e32 v33, v150, v33
	v_add_f32_e32 v33, v151, v33
	v_add_f32_e32 v33, v158, v33
	v_add_f32_e32 v33, v153, v33
	s_waitcnt lgkmcnt(1)
	v_mfma_f32_32x32x16_bf16 v[16:31], v[22:25], v[18:21], 0
	v_add_f32_e32 v33, v157, v33
	v_add_f32_e32 v33, v154, v33
	v_add_f32_e32 v33, v156, v33
	v_readlane_b32 s0, v254, 59
	v_add_f32_e32 v33, v155, v33
	s_add_i32 s0, s0, s51
	v_add_f32_e32 v180, v37, v33
	s_waitcnt lgkmcnt(0)
	v_mfma_f32_32x32x16_bf16 v[16:31], v[38:41], v[42:45], v[16:31]
	v_add_u32_e32 v33, s0, v34
	v_subrev_u32_e32 v33, s50, v33
	s_movk_i32 s0, 0x90
	v_mul_lo_u32 v33, v33, s0
	s_lshl_b32 s0, s51, 1
	v_add3_u32 v32, v32, v35, s0
	s_lshl_b32 s0, s50, 1
	v_xor_b32_e32 v172, 0x80000000, v170
	v_subrev_u32_e32 v32, s0, v32
	v_readlane_b32 s0, v255, 8
	v_readlane_b32 s52, v254, 21
	v_mov_b32_e32 v171, v170
	s_sub_i32 s33, s33, 64
	s_sub_i32 s38, s21, 31
	v_mov_b32_e32 v173, v172
	v_add3_u32 v181, v33, v35, 0
	v_add_u32_e32 v182, s0, v32
	v_add_u32_e32 v182, 0x12140, v182
	v_subrev_u32_e32 v183, 64, v36
	v_cvt_f32_i32_e32 v185, v183
	s_mov_b32 s39, 0
	s_movk_i32 s40, 0xfec0
	v_readlane_b32 s53, v254, 22
	s_branch .LBB0_261
.LBB0_259:
	v_exp_f32_e32 v32, v32
	v_exp_f32_e32 v163, v33
	v_exp_f32_e32 v164, v35
	v_exp_f32_e32 v35, v38
	v_add_f32_e32 v33, v163, v32
	v_exp_f32_e32 v162, v34
	v_exp_f32_e32 v34, v36
	v_exp_f32_e32 v36, v37
	v_exp_f32_e32 v37, v39
	v_add_f32_e32 v33, v162, v33
	v_add_f32_e32 v33, v164, v33
	v_add_f32_e32 v33, v34, v33
	v_exp_f32_e32 v38, v40
	v_add_f32_e32 v33, v36, v33
	v_exp_f32_e32 v39, v41
	v_add_f32_e32 v33, v35, v33
	v_exp_f32_e32 v40, v42
	v_add_f32_e32 v33, v37, v33
	v_exp_f32_e32 v41, v43
	v_add_f32_e32 v33, v38, v33
	v_exp_f32_e32 v42, v44
	v_add_f32_e32 v33, v39, v33
	v_exp_f32_e32 v43, v45
	v_add_f32_e32 v33, v40, v33
	v_exp_f32_e32 v44, v46
	v_add_f32_e32 v33, v41, v33
	v_exp_f32_e32 v45, v47
	v_add_f32_e32 v33, v42, v33
	v_add_f32_e32 v33, v43, v33
	v_add_f32_e32 v33, v44, v33
	v_add_f32_e32 v46, v45, v33
	v_cvt_pk_bf16_f32 v35, v35, v37
	v_cvt_pk_bf16_f32 v34, v34, v36
	v_cvt_pk_bf16_f32 v33, v162, v164
	v_cvt_pk_bf16_f32 v32, v32, v163
	v_add_f32_e32 v180, v180, v46
	s_waitcnt lgkmcnt(3)
	v_mfma_f32_32x32x16_bf16 v[0:15], v[150:153], v[32:35], v[0:15]
	s_waitcnt lgkmcnt(2)
	v_mfma_f32_32x32x16_bf16 v[16:31], v[146:149], v[32:35], v[16:31]
	v_cvt_pk_bf16_f32 v35, v44, v45
	v_cvt_pk_bf16_f32 v34, v42, v43
	v_cvt_pk_bf16_f32 v33, v40, v41
	v_cvt_pk_bf16_f32 v32, v38, v39
	s_waitcnt lgkmcnt(1)
	s_nop 0
	v_mfma_f32_32x32x16_bf16 v[0:15], v[158:161], v[32:35], v[0:15]
	s_waitcnt lgkmcnt(0)
	v_mfma_f32_32x32x16_bf16 v[16:31], v[154:157], v[32:35], v[16:31]
.LBB0_260:
	s_add_i32 s39, s39, 1
	s_add_i32 s40, s40, 64
	s_add_i32 s33, s33, 32
	v_add_u32_e32 v181, 0x1200, v181
	s_cmp_eq_u32 s40, 0
	v_add_f32_e32 v185, 0x42000000, v185
	s_cbranch_scc1 .LBB0_271
.LBB0_261:
	s_cmpk_eq_i32 s40, 0xff40
	s_cbranch_scc1 .LBB0_260
	s_cmpk_lt_i32 s33, 0xffe1
	s_cselect_b64 s[0:1], -1, 0
	s_cmp_ge_i32 s33, s21
	s_cselect_b64 s[36:37], -1, 0
	s_or_b64 s[0:1], s[0:1], s[36:37]
	s_and_b64 vcc, exec, s[0:1]
	s_cbranch_vccnz .LBB0_260
	ds_read_b128 v[166:169], v181
	ds_read_b128 v[162:165], v181 offset:32
	ds_read_b128 v[158:161], v181 offset:64
	ds_read_b128 v[154:157], v181 offset:96
	v_add_u32_e32 v184, s40, v182
	ds_read_b128 v[150:153], v184
	ds_read_b128 v[146:149], v184 offset:33280
	s_cmp_gt_u32 s39, 1
	s_mov_b64 s[0:1], -1
	s_cbranch_scc0 .LBB0_265
	v_fma_f32 v46, -v170, v185, -v178
	v_fmamk_f32 v32, v170, 0x80000000, v46
	v_sub_f32_e32 v33, v46, v170
	v_pk_fma_f32 v[34:35], v[172:173], s[28:29], v[46:47] op_sel_hi:[1,1,0]
	v_pk_fma_f32 v[36:37], v[172:173], s[84:85], v[46:47] op_sel_hi:[1,1,0]
	v_pk_fma_f32 v[38:39], v[172:173], s[82:83], v[46:47] op_sel_hi:[1,1,0]
	v_pk_fma_f32 v[40:41], v[172:173], s[26:27], v[46:47] op_sel_hi:[1,1,0]
	v_pk_fma_f32 v[42:43], v[172:173], s[24:25], v[46:47] op_sel_hi:[1,1,0]
	v_pk_fma_f32 v[44:45], v[172:173], s[86:87], v[46:47] op_sel_hi:[1,1,0]
	v_pk_fma_f32 v[46:47], v[172:173], s[2:3], v[46:47] op_sel_hi:[1,1,0]
	s_mov_b64 s[0:1], 0

.LBB0_267:
	s_and_b32 s41, s39, 3
	s_cmp_lt_i32 s33, 0
	s_cselect_b64 s[0:1], -1, 0
	s_cmp_ge_i32 s33, s38
	s_cselect_b64 s[36:37], -1, 0
	s_cmp_eq_u32 s41, 0
	s_cselect_b64 s[50:51], -1, 0
	s_or_b64 s[0:1], s[50:51], s[0:1]
	s_or_b64 s[0:1], s[0:1], s[36:37]
	s_andn2_b64 vcc, exec, s[0:1]
	s_cbranch_vccnz .LBB0_269
	v_cmp_nge_f32_e32 vcc, v185, v177
	v_cmp_nle_f32_e64 s[36:37], v185, v176
	s_or_b64 vcc, vcc, s[36:37]
	v_add_f32_e32 v186, 1.0, v185
	v_cndmask_b32_e32 v32, v32, v237, vcc
	v_cmp_nge_f32_e32 vcc, v186, v177
	v_cmp_nle_f32_e64 s[36:37], v186, v176
	s_or_b64 vcc, vcc, s[36:37]
	v_add_f32_e32 v186, 2.0, v185
	v_cndmask_b32_e32 v33, v33, v237, vcc
	v_cmp_nge_f32_e32 vcc, v186, v177
	v_cmp_nle_f32_e64 s[36:37], v186, v176
	s_or_b64 vcc, vcc, s[36:37]
	v_add_f32_e32 v186, 0x40400000, v185
	v_cndmask_b32_e32 v34, v34, v237, vcc
	v_cmp_nge_f32_e32 vcc, v186, v177
	v_cmp_nle_f32_e64 s[36:37], v186, v176
	s_or_b64 vcc, vcc, s[36:37]
	v_add_f32_e32 v186, 0x41000000, v185
	v_cndmask_b32_e32 v35, v35, v237, vcc
	v_cmp_nge_f32_e32 vcc, v186, v177
	v_cmp_nle_f32_e64 s[36:37], v186, v176
	s_or_b64 vcc, vcc, s[36:37]
	v_add_f32_e32 v186, 0x41100000, v185
	v_cndmask_b32_e32 v36, v36, v237, vcc
	v_cmp_nge_f32_e32 vcc, v186, v177
	v_cmp_nle_f32_e64 s[36:37], v186, v176
	s_or_b64 vcc, vcc, s[36:37]
	v_add_f32_e32 v186, 0x41200000, v185
	v_cndmask_b32_e32 v37, v37, v237, vcc
	v_cmp_nge_f32_e32 vcc, v186, v177
	v_cmp_nle_f32_e64 s[36:37], v186, v176
	s_or_b64 vcc, vcc, s[36:37]
	v_add_f32_e32 v186, 0x41300000, v185
	v_cndmask_b32_e32 v38, v38, v237, vcc
	v_cmp_nge_f32_e32 vcc, v186, v177
	v_cmp_nle_f32_e64 s[36:37], v186, v176
	s_or_b64 vcc, vcc, s[36:37]
	v_add_f32_e32 v186, 0x41800000, v185
	v_cndmask_b32_e32 v39, v39, v237, vcc
	v_cmp_nge_f32_e32 vcc, v186, v177
	v_cmp_nle_f32_e64 s[36:37], v186, v176
	s_or_b64 vcc, vcc, s[36:37]
	v_add_f32_e32 v186, 0x41880000, v185
	v_cndmask_b32_e32 v40, v40, v237, vcc
	v_cmp_nge_f32_e32 vcc, v186, v177
	v_cmp_nle_f32_e64 s[36:37], v186, v176
	s_or_b64 vcc, vcc, s[36:37]
	v_add_f32_e32 v186, 0x41900000, v185
	v_cndmask_b32_e32 v41, v41, v237, vcc
	v_cmp_nge_f32_e32 vcc, v186, v177
	v_cmp_nle_f32_e64 s[36:37], v186, v176
	s_or_b64 vcc, vcc, s[36:37]
	v_add_f32_e32 v186, 0x41980000, v185
	v_cndmask_b32_e32 v42, v42, v237, vcc
	v_cmp_nge_f32_e32 vcc, v186, v177
	v_cmp_nle_f32_e64 s[36:37], v186, v176
	s_or_b64 vcc, vcc, s[36:37]
	v_add_f32_e32 v186, 0x41c00000, v185
	v_cndmask_b32_e32 v43, v43, v237, vcc
	v_cmp_nge_f32_e32 vcc, v186, v177
	v_cmp_nle_f32_e64 s[36:37], v186, v176
	s_or_b64 vcc, vcc, s[36:37]
	v_add_f32_e32 v186, 0x41c80000, v185
	v_cndmask_b32_e32 v44, v44, v237, vcc
	v_cmp_nge_f32_e32 vcc, v186, v177
	v_cmp_nle_f32_e64 s[36:37], v186, v176
	s_or_b64 vcc, vcc, s[36:37]
	v_add_f32_e32 v186, 0x41d00000, v185
	v_cndmask_b32_e32 v45, v45, v237, vcc
	v_cmp_nge_f32_e32 vcc, v186, v177
	v_cmp_nle_f32_e64 s[36:37], v186, v176
	s_or_b64 vcc, vcc, s[36:37]
	v_add_f32_e32 v186, 0x41d80000, v185
	v_cndmask_b32_e32 v46, v46, v237, vcc
	v_cmp_nge_f32_e32 vcc, v186, v177
	v_cmp_nle_f32_e64 s[36:37], v186, v176
	s_or_b64 vcc, vcc, s[36:37]
	v_cndmask_b32_e32 v47, v47, v237, vcc
.LBB0_269:
	s_waitcnt lgkmcnt(5)
	s_nop 0
	v_mfma_f32_32x32x16_bf16 v[32:47], v[166:169], v[50:53], v[32:47]
	s_waitcnt lgkmcnt(4)
	v_mfma_f32_32x32x16_bf16 v[32:47], v[162:165], v[54:57], v[32:47]
	s_waitcnt lgkmcnt(3)
	v_mfma_f32_32x32x16_bf16 v[32:47], v[158:161], v[58:61], v[32:47]
	s_waitcnt lgkmcnt(2)
	v_mfma_f32_32x32x16_bf16 v[32:47], v[154:157], v[62:65], v[32:47]
	ds_read_b128 v[158:161], v184 offset:32
	ds_read_b128 v[154:157], v184 offset:33312
	s_nop 9
	v_max3_f32 v162, v32, v33, v34
	v_max3_f32 v162, v162, v35, v36
	v_max3_f32 v162, v162, v37, v38
	v_max3_f32 v162, v162, v39, v40
	v_max3_f32 v162, v162, v41, v42
	v_max3_f32 v162, v162, v43, v44
	v_max3_f32 v162, v162, v45, v46
	v_max_f32_e32 v162, v162, v47
	v_cmp_lt_f32_e32 vcc, s84, v162
	s_cbranch_vccz .LBB0_259
	v_max_f32_e32 v162, v162, v162
	v_max_f32_e32 v162, 0, v162
	ds_bpermute_b32 v163, v179, v162
	s_waitcnt lgkmcnt(0)
	v_max_f32_e32 v163, v163, v163
	v_max_f32_e32 v162, v162, v163
	v_exp_f32_e64 v164, -v162
	v_pk_add_f32 v[32:33], v[32:33], v[162:163] op_sel_hi:[1,0] neg_lo:[0,1] neg_hi:[0,1]
	v_pk_add_f32 v[34:35], v[34:35], v[162:163] op_sel_hi:[1,0] neg_lo:[0,1] neg_hi:[0,1]
	v_pk_add_f32 v[36:37], v[36:37], v[162:163] op_sel_hi:[1,0] neg_lo:[0,1] neg_hi:[0,1]
	v_pk_add_f32 v[38:39], v[38:39], v[162:163] op_sel_hi:[1,0] neg_lo:[0,1] neg_hi:[0,1]
	v_pk_add_f32 v[40:41], v[40:41], v[162:163] op_sel_hi:[1,0] neg_lo:[0,1] neg_hi:[0,1]
	v_pk_add_f32 v[42:43], v[42:43], v[162:163] op_sel_hi:[1,0] neg_lo:[0,1] neg_hi:[0,1]
	v_pk_add_f32 v[44:45], v[44:45], v[162:163] op_sel_hi:[1,0] neg_lo:[0,1] neg_hi:[0,1]
	v_pk_add_f32 v[46:47], v[46:47], v[162:163] op_sel_hi:[1,0] neg_lo:[0,1] neg_hi:[0,1]
	v_pk_mul_f32 v[14:15], v[14:15], v[164:165] op_sel_hi:[1,0]
	v_pk_mul_f32 v[12:13], v[12:13], v[164:165] op_sel_hi:[1,0]
	v_pk_mul_f32 v[10:11], v[10:11], v[164:165] op_sel_hi:[1,0]
	v_pk_mul_f32 v[8:9], v[8:9], v[164:165] op_sel_hi:[1,0]
	v_pk_mul_f32 v[6:7], v[6:7], v[164:165] op_sel_hi:[1,0]
	v_pk_mul_f32 v[4:5], v[4:5], v[164:165] op_sel_hi:[1,0]
	v_pk_mul_f32 v[2:3], v[2:3], v[164:165] op_sel_hi:[1,0]
	v_pk_mul_f32 v[0:1], v[0:1], v[164:165] op_sel_hi:[1,0]
	v_pk_mul_f32 v[30:31], v[30:31], v[164:165] op_sel_hi:[1,0]
	v_pk_mul_f32 v[28:29], v[28:29], v[164:165] op_sel_hi:[1,0]
	v_pk_mul_f32 v[26:27], v[26:27], v[164:165] op_sel_hi:[1,0]
	v_pk_mul_f32 v[24:25], v[24:25], v[164:165] op_sel_hi:[1,0]
	v_pk_mul_f32 v[22:23], v[22:23], v[164:165] op_sel_hi:[1,0]
	v_pk_mul_f32 v[20:21], v[20:21], v[164:165] op_sel_hi:[1,0]
	v_pk_mul_f32 v[18:19], v[18:19], v[164:165] op_sel_hi:[1,0]
	v_pk_mul_f32 v[16:17], v[16:17], v[164:165] op_sel_hi:[1,0]
	v_mul_f32_e32 v180, v180, v164
	v_add_f32_e32 v178, v178, v162
	s_branch .LBB0_259

.LBB0_329:
	s_add_i32 s14, s18, 1
	v_readlane_b32 s22, v254, 34
	s_cmp_ge_i32 s14, s22
	s_cselect_b64 s[70:71], -1, 0
	s_cmp_lt_i32 s14, s22
	s_cselect_b64 s[72:73], -1, 0
	s_and_b64 s[0:1], s[72:73], exec
	s_cselect_b32 s19, s14, s18
	s_lshl_b32 s0, s19, 4
	s_and_b32 s0, s0, 0x180
	s_add_u32 s4, s8, s0
	s_addc_u32 s5, s9, 0
	s_add_u32 s0, s10, s0
	s_addc_u32 s1, s12, 0
	s_lshl_b32 s20, s19, 6
	s_lshl_b32 s19, s19, 8
	s_waitcnt vmcnt(6)
	v_mov_b32_e32 v4, v240
	s_and_b32 s19, s19, 0x700
	s_add_i32 s21, s19, 0xffffff80
	v_ashrrev_i32_e32 v0, 3, v4
	v_lshlrev_b32_e32 v2, 4, v4
	v_add_u32_e32 v5, 0x200, v4
	v_min_i32_e32 v0, 0x1ff, v0
	v_and_b32_e32 v48, 0x70, v2
	v_ashrrev_i32_e32 v2, 3, v5
	v_add_u32_e32 v0, s21, v0
	v_min_i32_e32 v2, 0x1ff, v2
	s_and_b32 s16, s20, 0xfffff800
	v_med3_i32 v0, v0, 0, v236
	v_add_u32_e32 v2, s21, v2
	v_or_b32_e32 v0, s16, v0
	v_med3_i32 v2, v2, 0, v236
	v_ashrrev_i32_e32 v1, 31, v0
	v_or_b32_e32 v2, s16, v2
	v_lshlrev_b64 v[0:1], 9, v[0:1]
	v_ashrrev_i32_e32 v3, 31, v2
	v_lshl_add_u64 v[0:1], s[4:5], 0, v[0:1]
	v_lshlrev_b64 v[2:3], 9, v[2:3]
	v_lshl_add_u64 v[0:1], v[0:1], 0, v[48:49]
	v_lshl_add_u64 v[2:3], s[4:5], 0, v[2:3]
	v_lshl_add_u64 v[2:3], v[2:3], 0, v[48:49]
	global_load_dwordx4 v[142:145], v[0:1], off
	global_load_dwordx4 v[126:129], v[2:3], off
	v_add_u32_e32 v0, 0x400, v4
	v_ashrrev_i32_e32 v0, 3, v0
	v_add_u32_e32 v2, 0x600, v4
	v_min_i32_e32 v0, 0x1ff, v0
	v_ashrrev_i32_e32 v2, 3, v2
	v_add_u32_e32 v0, s21, v0
	v_min_i32_e32 v2, 0x1ff, v2
	v_med3_i32 v0, v0, 0, v236
	v_add_u32_e32 v2, s21, v2
	v_or_b32_e32 v0, s16, v0
	v_med3_i32 v2, v2, 0, v236
	v_ashrrev_i32_e32 v1, 31, v0
	v_or_b32_e32 v2, s16, v2
	v_lshlrev_b64 v[0:1], 9, v[0:1]
	v_ashrrev_i32_e32 v3, 31, v2
	v_lshl_add_u64 v[0:1], s[4:5], 0, v[0:1]
	v_lshlrev_b64 v[2:3], 9, v[2:3]
	v_lshl_add_u64 v[0:1], v[0:1], 0, v[48:49]
	v_lshl_add_u64 v[2:3], s[4:5], 0, v[2:3]
	v_lshl_add_u64 v[2:3], v[2:3], 0, v[48:49]
	global_load_dwordx4 v[138:141], v[0:1], off
	global_load_dwordx4 v[122:125], v[2:3], off
	v_add_u32_e32 v0, 0x800, v4
	v_ashrrev_i32_e32 v0, 3, v0
	v_add_u32_e32 v2, 0xa00, v4
	v_min_i32_e32 v0, 0x1ff, v0
	v_ashrrev_i32_e32 v2, 3, v2
	v_add_u32_e32 v0, s21, v0
	v_min_i32_e32 v2, 0x1ff, v2
	v_med3_i32 v0, v0, 0, v236
	v_add_u32_e32 v2, s21, v2
	v_or_b32_e32 v0, s16, v0
	v_med3_i32 v2, v2, 0, v236
	v_ashrrev_i32_e32 v1, 31, v0
	v_or_b32_e32 v2, s16, v2
	v_lshlrev_b64 v[0:1], 9, v[0:1]
	v_ashrrev_i32_e32 v3, 31, v2
	v_lshl_add_u64 v[0:1], s[4:5], 0, v[0:1]
	v_lshlrev_b64 v[2:3], 9, v[2:3]
	v_lshl_add_u64 v[0:1], v[0:1], 0, v[48:49]
	v_lshl_add_u64 v[2:3], s[4:5], 0, v[2:3]
	v_lshl_add_u64 v[2:3], v[2:3], 0, v[48:49]
	global_load_dwordx4 v[134:137], v[0:1], off
	global_load_dwordx4 v[118:121], v[2:3], off
	v_add_u32_e32 v0, 0xc00, v4
	v_ashrrev_i32_e32 v0, 3, v0
	v_add_u32_e32 v2, 0xe00, v4
	v_min_i32_e32 v0, 0x1ff, v0
	v_ashrrev_i32_e32 v2, 3, v2
	v_add_u32_e32 v0, s21, v0
	v_min_i32_e32 v2, 0x1ff, v2
	v_med3_i32 v0, v0, 0, v236
	v_add_u32_e32 v2, s21, v2
	v_or_b32_e32 v0, s16, v0
	v_med3_i32 v2, v2, 0, v236
	v_ashrrev_i32_e32 v1, 31, v0
	v_or_b32_e32 v2, s16, v2
	v_lshlrev_b64 v[0:1], 9, v[0:1]
	v_ashrrev_i32_e32 v3, 31, v2
	v_lshl_add_u64 v[0:1], s[4:5], 0, v[0:1]
	v_lshlrev_b64 v[2:3], 9, v[2:3]
	v_lshl_add_u64 v[0:1], v[0:1], 0, v[48:49]
	v_lshl_add_u64 v[2:3], s[4:5], 0, v[2:3]
	v_lshl_add_u64 v[2:3], v[2:3], 0, v[48:49]
	global_load_dwordx4 v[130:133], v[0:1], off
	global_load_dwordx4 v[114:117], v[2:3], off
	v_ashrrev_i32_e32 v0, 1, v4
	v_and_b32_e32 v0, -4, v0
	s_movk_i32 s4, 0x200
	v_add_u32_e32 v1, 0xffffff80, v0
	v_cmp_gt_i32_e32 vcc, s4, v0
	s_nop 1
	v_cndmask_b32_e32 v0, v238, v1, vcc
	v_add_u32_e32 v4, s19, v0
	v_max_i32_e32 v2, -1, v4
	v_med3_i32 v0, v4, 0, v236
	v_add_u32_e32 v2, 1, v2
	v_or_b32_e32 v0, s16, v0
	v_min_u32_e32 v2, 0x7ff, v2
	v_ashrrev_i32_e32 v1, 31, v0
	v_or_b32_e32 v2, s16, v2
	v_lshlrev_b64 v[0:1], 9, v[0:1]
	v_ashrrev_i32_e32 v3, 31, v2
	v_lshl_add_u64 v[0:1], s[0:1], 0, v[0:1]
	v_lshlrev_b64 v[2:3], 9, v[2:3]
	v_lshl_add_u64 v[0:1], v[0:1], 0, v[48:49]
	v_lshl_add_u64 v[2:3], s[0:1], 0, v[2:3]
	v_lshl_add_u64 v[2:3], v[2:3], 0, v[48:49]
	global_load_dwordx4 v[74:77], v[0:1], off
	global_load_dwordx4 v[78:81], v[2:3], off
	v_max_i32_e32 v0, -2, v4
	v_add_u32_e32 v0, 2, v0
	v_max_i32_e32 v2, -3, v4
	v_min_u32_e32 v0, 0x7ff, v0
	v_add_u32_e32 v2, 3, v2
	v_or_b32_e32 v0, s16, v0
	v_min_u32_e32 v2, 0x7ff, v2
	v_ashrrev_i32_e32 v1, 31, v0
	v_or_b32_e32 v2, s16, v2
	v_lshlrev_b64 v[0:1], 9, v[0:1]
	v_ashrrev_i32_e32 v3, 31, v2
	v_lshl_add_u64 v[0:1], s[0:1], 0, v[0:1]
	v_lshlrev_b64 v[2:3], 9, v[2:3]
	v_lshl_add_u64 v[0:1], v[0:1], 0, v[48:49]
	v_lshl_add_u64 v[2:3], s[0:1], 0, v[2:3]
	v_lshl_add_u64 v[2:3], v[2:3], 0, v[48:49]
	global_load_dwordx4 v[110:113], v[0:1], off
	global_load_dwordx4 v[106:109], v[2:3], off
	v_ashrrev_i32_e32 v0, 1, v5
	v_and_b32_e32 v0, -4, v0
	v_add_u32_e32 v1, 0xffffff80, v0
	v_cmp_gt_i32_e32 vcc, s4, v0
	v_readlane_b32 s4, v255, 10
	s_nop 0
	v_cndmask_b32_e32 v0, v238, v1, vcc
	v_add_u32_e32 v4, s19, v0
	v_max_i32_e32 v2, -1, v4
	v_add_u32_e32 v2, 1, v2
	v_med3_i32 v0, v4, 0, v236
	v_min_u32_e32 v2, 0x7ff, v2
	v_or_b32_e32 v0, s16, v0
	v_or_b32_e32 v2, s16, v2
	v_ashrrev_i32_e32 v1, 31, v0
	v_ashrrev_i32_e32 v3, 31, v2
	v_lshlrev_b64 v[0:1], 9, v[0:1]
	v_lshlrev_b64 v[2:3], 9, v[2:3]
	v_lshl_add_u64 v[0:1], s[0:1], 0, v[0:1]
	v_lshl_add_u64 v[2:3], s[0:1], 0, v[2:3]
	v_lshl_add_u64 v[0:1], v[0:1], 0, v[48:49]
	v_lshl_add_u64 v[2:3], v[2:3], 0, v[48:49]
	global_load_dwordx4 v[66:69], v[0:1], off
	global_load_dwordx4 v[70:73], v[2:3], off
	v_max_i32_e32 v0, -2, v4
	v_max_i32_e32 v2, -3, v4
	v_add_u32_e32 v0, 2, v0
	v_add_u32_e32 v2, 3, v2
	v_min_u32_e32 v0, 0x7ff, v0
	v_min_u32_e32 v2, 0x7ff, v2
	v_or_b32_e32 v0, s16, v0
	v_or_b32_e32 v2, s16, v2
	v_ashrrev_i32_e32 v1, 31, v0
	v_ashrrev_i32_e32 v3, 31, v2
	v_lshlrev_b64 v[0:1], 9, v[0:1]
	v_lshlrev_b64 v[2:3], 9, v[2:3]
	v_lshl_add_u64 v[0:1], s[0:1], 0, v[0:1]
	v_lshl_add_u64 v[2:3], s[0:1], 0, v[2:3]
	v_lshl_add_u64 v[0:1], v[0:1], 0, v[48:49]
	v_lshl_add_u64 v[2:3], v[2:3], 0, v[48:49]
	s_and_b32 s0, s20, 0x600
	global_load_dwordx4 v[86:89], v[0:1], off
	global_load_dwordx4 v[82:85], v[2:3], off
	s_add_u32 s0, s6, s0
	v_mov_b32_e32 v2, v239
	s_addc_u32 s1, s7, 0
	s_add_i32 s4, s4, s16
	v_and_or_b32 v0, v2, 31, s19
	v_add_u32_e32 v0, s4, v0
	v_ashrrev_i32_e32 v1, 31, v0
	v_ashrrev_i32_e32 v2, 2, v2
	v_lshlrev_b64 v[0:1], 11, v[0:1]
	v_and_b32_e32 v2, -8, v2
	v_lshl_add_u64 v[0:1], s[0:1], 0, v[0:1]
	v_ashrrev_i32_e32 v3, 31, v2
	v_lshl_add_u64 v[0:1], v[2:3], 1, v[0:1]
	global_load_dwordx4 v[90:93], v[0:1], off
	global_load_dwordx4 v[94:97], v[0:1], off offset:32
	global_load_dwordx4 v[98:101], v[0:1], off offset:64
	global_load_dwordx4 v[102:105], v[0:1], off offset:96
	s_cmp_eq_u32 s14, s22
	v_readlane_b32 s4, v254, 37
	s_cselect_b64 s[0:1], -1, 0
	v_readlane_b32 s5, v254, 38
	s_and_b64 s[0:1], s[4:5], s[0:1]
	s_and_b64 s[0:1], s[0:1], exec
	s_cselect_b32 s4, 4, 4
	v_readlane_b32 s0, v254, 30
	v_mov_b32_e32 v0, v239
	s_cmp_ge_u32 s0, s4
	s_cbranch_scc1 .LBB0_350
	s_and_b32 s0, s13, 0x700
	v_readlane_b32 s1, v255, 11
	s_add_i32 s5, s1, s0
	s_lshl_b32 s0, s18, 8
	s_and_b32 s0, s0, 0x700
	v_readlane_b32 s19, v255, 10
	s_bfe_u32 s1, s18, 0x20003
	v_and_b32_e32 v1, 31, v0
	s_add_i32 s19, s0, s19
	s_lshl_b32 s16, s1, 2
	v_or_b32_e32 v2, s19, v1
	s_lshl_b32 s0, s1, 9
	v_sub_u32_e32 v3, 0, v2
	s_add_u32 s0, s6, s0
	v_max_i32_e32 v3, 0xffffff80, v3
	s_addc_u32 s1, s7, 0
	s_lshl_b32 s18, s18, 6
	v_cvt_f32_i32_e32 v241, v3
	v_sub_u32_e32 v3, 0x7ff, v2
	s_and_b32 s18, s18, 0xfffff800
	v_min_i32_e32 v3, 0x80, v3
	v_add_u32_e32 v2, s18, v2
	v_cvt_f32_i32_e32 v242, v3
	v_ashrrev_i32_e32 v3, 31, v2
	v_lshlrev_b64 v[2:3], 11, v[2:3]
	s_cmp_lt_i32 s19, 0
	v_lshl_add_u64 v[206:207], s[0:1], 0, v[2:3]
	s_cselect_b64 s[0:1], -1, 0
	s_or_b32 s18, s19, 31
	v_ashrrev_i32_e32 v4, 5, v0
	s_cmpk_gt_i32 s18, 0x7ff
	s_cselect_b64 s[18:19], -1, 0
	v_lshlrev_b32_e32 v5, 2, v4
	s_or_b64 s[74:75], s[0:1], s[18:19]
	v_readlane_b32 s0, v254, 39
	v_sub_u32_e32 v5, v5, v1
	s_movk_i32 s19, 0x90
	v_or_b32_e32 v2, s0, v1
	v_lshlrev_b32_e32 v3, 4, v4
	v_cvt_f32_i32_e32 v48, v5
	v_readlane_b32 s0, v254, 40
	v_mul_lo_u32 v2, v2, s19
	v_lshlrev_b32_e32 v0, 2, v0
	v_add_u32_e32 v6, s0, v3
	v_readlane_b32 s0, v255, 16
	v_add3_u32 v2, 0, v2, v3
	v_xor_b32_e32 v243, 0x80, v0
	v_mul_u32_u24_e32 v0, 0x410, v1
	s_add_i32 s18, 0, 0x12000
	v_readlane_b32 s1, v255, 17
	v_lshlrev_b32_e32 v208, 3, v4
	s_mov_b32 s20, s0
	s_mov_b32 s21, s28
	v_writelane_b32 v255, s0, 16
	v_add3_u32 v4, s18, v0, v6
	ds_read_b128 v[146:149], v2
	ds_read_b128 v[150:153], v2 offset:32
	ds_read_b128 v[154:157], v2 offset:64
	ds_read_b128 v[158:161], v2 offset:96
	ds_read_b128 v[162:165], v4
	ds_read_b128 v[166:169], v4 offset:32
	ds_read_b128 v[170:173], v4 offset:33280
	ds_read_b128 v[174:177], v4 offset:33312
	v_cmp_nge_f32_e32 vcc, v48, v241
	v_cmp_nle_f32_e64 s[36:37], v48, v242
	v_writelane_b32 v255, s1, 17
	v_pk_add_f32 v[210:211], v[48:49], s[20:21] op_sel_hi:[0,1]
	s_mov_b32 s0, s29
	s_mov_b32 s1, s84
	s_or_b64 s[36:37], vcc, s[36:37]
	v_cmp_nge_f32_e32 vcc, v210, v241
	v_cmp_nge_f32_e64 s[38:39], v211, v241
	v_cmp_nle_f32_e64 s[40:41], v210, v242
	v_cmp_nle_f32_e64 s[42:43], v211, v242
	v_pk_add_f32 v[212:213], v[48:49], s[0:1] op_sel_hi:[0,1]
	s_mov_b32 s0, s85
	s_mov_b32 s1, s82
	s_or_b64 s[38:39], s[38:39], s[42:43]
	s_or_b64 s[40:41], vcc, s[40:41]
	v_cmp_nge_f32_e32 vcc, v212, v241
	v_cmp_nge_f32_e64 s[42:43], v213, v241
	v_cmp_nle_f32_e64 s[44:45], v212, v242
	v_cmp_nle_f32_e64 s[46:47], v213, v242
	v_pk_add_f32 v[214:215], v[48:49], s[0:1] op_sel_hi:[0,1]
	s_mov_b32 s0, s83
	s_mov_b32 s1, s26
	s_or_b64 s[42:43], s[42:43], s[46:47]
	s_or_b64 s[44:45], vcc, s[44:45]
	v_cmp_nge_f32_e32 vcc, v214, v241
	v_cmp_nge_f32_e64 s[46:47], v215, v241
	v_cmp_nle_f32_e64 s[48:49], v214, v242
	v_cmp_nle_f32_e64 s[50:51], v215, v242
	v_pk_add_f32 v[216:217], v[48:49], s[0:1] op_sel_hi:[0,1]
	s_mov_b32 s0, s27
	s_mov_b32 s1, s24
	s_or_b64 s[46:47], s[46:47], s[50:51]
	s_or_b64 s[48:49], vcc, s[48:49]
	v_cmp_nge_f32_e32 vcc, v216, v241
	v_cmp_nge_f32_e64 s[50:51], v217, v241
	v_cmp_nle_f32_e64 s[52:53], v216, v242
	v_cmp_nle_f32_e64 s[54:55], v217, v242
	v_pk_add_f32 v[218:219], v[48:49], s[0:1] op_sel_hi:[0,1]
	s_mov_b32 s0, s25
	s_mov_b32 s1, s86
	s_or_b64 s[50:51], s[50:51], s[54:55]
	s_or_b64 s[52:53], vcc, s[52:53]
	v_cmp_nge_f32_e32 vcc, v218, v241
	v_cmp_nge_f32_e64 s[54:55], v219, v241
	v_cmp_nle_f32_e64 s[56:57], v218, v242
	v_cmp_nle_f32_e64 s[58:59], v219, v242
	v_pk_add_f32 v[220:221], v[48:49], s[0:1] op_sel_hi:[0,1]
	s_mov_b32 s0, s87
	s_mov_b32 s1, s2
	s_or_b64 s[54:55], s[54:55], s[58:59]
	s_or_b64 s[56:57], vcc, s[56:57]
	v_cmp_nge_f32_e32 vcc, v220, v241
	v_cmp_nge_f32_e64 s[58:59], v221, v241
	v_cmp_nle_f32_e64 s[60:61], v220, v242
	v_cmp_nle_f32_e64 s[62:63], v221, v242
	v_pk_add_f32 v[222:223], v[48:49], s[0:1] op_sel_hi:[0,1]
	v_readlane_b32 s0, v254, 60
	v_add_f32_e32 v244, 0x41d80000, v48
	s_or_b64 s[58:59], s[58:59], s[62:63]
	s_or_b64 s[60:61], vcc, s[60:61]
	v_cmp_nge_f32_e32 vcc, v222, v241
	v_cmp_nge_f32_e64 s[62:63], v223, v241
	v_cmp_nle_f32_e64 s[64:65], v222, v242
	v_cmp_nle_f32_e64 s[66:67], v223, v242
	v_add_u32_e32 v1, s0, v1
	s_or_b64 s[62:63], s[62:63], s[66:67]
	s_or_b64 s[64:65], vcc, s[64:65]
	v_cmp_nge_f32_e32 vcc, v244, v241
	v_cmp_nle_f32_e64 s[66:67], v244, v242
	v_mul_lo_u32 v1, v1, s19
	v_readlane_b32 s0, v254, 61
	v_ashrrev_i32_e32 v209, 31, v208
	s_or_b64 s[66:67], vcc, s[66:67]
	v_add3_u32 v245, v1, v3, 0
	v_add3_u32 v246, v0, v3, s0
	v_add_u32_e32 v246, 0x12240, v246
	v_add_u32_e32 v247, 0xffffff80, v5
	v_readlane_b32 s18, v254, 30
	s_branch .LBB0_332

.LBB0_334:
	v_max_f32_e32 v10, v0, v0
	v_max_f32_e32 v11, v20, v20
	v_max_f32_e32 v10, v11, v10
	v_max3_f32 v10, v10, v1, v2
	v_max3_f32 v10, v10, v3, v4
	v_max3_f32 v10, v10, v5, v6
	v_max3_f32 v10, v10, v7, v8
	v_max3_f32 v10, v10, v9, v16
	v_max3_f32 v10, v10, v17, v18
	v_max3_f32 v10, v10, v19, v21
	ds_bpermute_b32 v11, v243, v10
	v_xor_b32_e32 v226, 0x80000000, v224
	v_mov_b32_e32 v225, v224
	v_mov_b32_e32 v227, v226
	s_mov_b32 s19, 0
	s_waitcnt lgkmcnt(0)
	v_max_f32_e32 v11, v11, v11
	v_max_f32_e32 v249, v10, v11
	v_sub_f32_e32 v0, v0, v249
	v_exp_f32_e32 v37, v0
	v_sub_f32_e32 v0, v2, v249
	v_exp_f32_e32 v39, v0
	v_sub_f32_e32 v0, v3, v249
	v_exp_f32_e32 v40, v0
	v_sub_f32_e32 v0, v4, v249
	v_exp_f32_e32 v41, v0
	v_sub_f32_e32 v0, v5, v249
	v_sub_f32_e32 v10, v20, v249
	v_sub_f32_e32 v1, v1, v249
	v_exp_f32_e32 v42, v0
	v_sub_f32_e32 v0, v6, v249
	v_exp_f32_e32 v36, v10
	v_exp_f32_e32 v38, v1
	v_exp_f32_e32 v43, v0
	v_sub_f32_e32 v33, v16, v249
	v_sub_f32_e32 v16, v17, v249
	v_sub_f32_e32 v0, v7, v249
	v_exp_f32_e32 v46, v16
	v_sub_f32_e32 v16, v19, v249
	v_exp_f32_e32 v44, v0
	v_sub_f32_e32 v0, v9, v249
	v_cvt_pk_bf16_f32 v25, v42, v43
	v_cvt_pk_bf16_f32 v24, v40, v41
	v_cvt_pk_bf16_f32 v23, v38, v39
	v_cvt_pk_bf16_f32 v22, v36, v37
	v_exp_f32_e32 v47, v16
	v_sub_f32_e32 v16, v21, v249
	v_sub_f32_e32 v32, v8, v249
	v_exp_f32_e32 v45, v0
	v_mfma_f32_32x32x16_bf16 v[0:15], v[162:165], v[22:25], 0
	v_sub_f32_e32 v34, v18, v249
	v_exp_f32_e32 v178, v16
	v_exp_f32_e32 v179, v34
	v_exp_f32_e32 v180, v33
	v_exp_f32_e32 v181, v32
	v_cvt_pk_bf16_f32 v35, v47, v178
	v_cvt_pk_bf16_f32 v34, v46, v179
	v_mfma_f32_32x32x16_bf16 v[16:31], v[170:173], v[22:25], 0
	v_cvt_pk_bf16_f32 v33, v45, v180
	v_cvt_pk_bf16_f32 v32, v44, v181
	s_movk_i32 s20, 0xfdc0
	s_mov_b32 s21, s5
	v_cvt_f32_i32_e32 v234, v247
	v_mov_b32_e32 v252, v245
	v_mfma_f32_32x32x16_bf16 v[0:15], v[166:169], v[32:35], v[0:15]
	v_mfma_f32_32x32x16_bf16 v[16:31], v[174:177], v[32:35], v[16:31]
	v_add_f32_e32 v32, 0, v36
	v_add_f32_e32 v32, v37, v32
	v_add_f32_e32 v32, v38, v32
	v_add_f32_e32 v32, v39, v32
	v_add_f32_e32 v32, v40, v32
	v_add_f32_e32 v32, v41, v32
	v_add_f32_e32 v32, v42, v32
	v_add_f32_e32 v32, v43, v32
	v_add_f32_e32 v32, v44, v32
	v_add_f32_e32 v32, v181, v32
	v_add_f32_e32 v32, v45, v32
	v_add_f32_e32 v32, v180, v32
	v_add_f32_e32 v32, v46, v32
	v_add_f32_e32 v32, v179, v32
	v_add_f32_e32 v32, v47, v32
	v_add_f32_e32 v250, v178, v32
	s_branch .LBB0_337
.LBB0_335:
	v_exp_f32_e32 v32, v32
	v_exp_f32_e32 v195, v33
	v_exp_f32_e32 v196, v35
	v_exp_f32_e32 v35, v38
	v_add_f32_e32 v33, v195, v32
	v_exp_f32_e32 v194, v34
	v_exp_f32_e32 v34, v36
	v_exp_f32_e32 v36, v37
	v_exp_f32_e32 v37, v39
	v_add_f32_e32 v33, v194, v33
	v_add_f32_e32 v33, v196, v33
	v_add_f32_e32 v33, v34, v33
	v_exp_f32_e32 v38, v40
	v_add_f32_e32 v33, v36, v33
	v_exp_f32_e32 v39, v41
	v_add_f32_e32 v33, v35, v33
	v_exp_f32_e32 v40, v42
	v_add_f32_e32 v33, v37, v33
	v_exp_f32_e32 v41, v43
	v_add_f32_e32 v33, v38, v33
	v_exp_f32_e32 v42, v44
	v_add_f32_e32 v33, v39, v33
	v_exp_f32_e32 v43, v45
	v_add_f32_e32 v33, v40, v33
	v_exp_f32_e32 v44, v46
	v_add_f32_e32 v33, v41, v33
	v_exp_f32_e32 v45, v47
	v_add_f32_e32 v33, v42, v33
	v_add_f32_e32 v33, v43, v33
	v_add_f32_e32 v33, v44, v33
	v_add_f32_e32 v46, v45, v33
	v_cvt_pk_bf16_f32 v35, v35, v37
	v_cvt_pk_bf16_f32 v34, v34, v36
	v_cvt_pk_bf16_f32 v33, v194, v196
	v_cvt_pk_bf16_f32 v32, v32, v195
	v_add_f32_e32 v250, v250, v46
	s_waitcnt lgkmcnt(3)
	v_mfma_f32_32x32x16_bf16 v[0:15], v[182:185], v[32:35], v[0:15]
	s_waitcnt lgkmcnt(2)
	v_mfma_f32_32x32x16_bf16 v[16:31], v[178:181], v[32:35], v[16:31]
	v_cvt_pk_bf16_f32 v35, v44, v45
	v_cvt_pk_bf16_f32 v34, v42, v43
	v_cvt_pk_bf16_f32 v33, v40, v41
	v_cvt_pk_bf16_f32 v32, v38, v39
	s_waitcnt lgkmcnt(1)
	s_nop 0
	v_mfma_f32_32x32x16_bf16 v[0:15], v[190:193], v[32:35], v[0:15]
	s_waitcnt lgkmcnt(0)
	v_mfma_f32_32x32x16_bf16 v[16:31], v[186:189], v[32:35], v[16:31]
.LBB0_336:
	s_add_i32 s19, s19, 1
	s_add_i32 s20, s20, 64
	s_add_i32 s21, s21, 32
	v_add_u32_e32 v252, 0x1200, v252
	s_cmp_eq_u32 s20, 0
	v_add_f32_e32 v234, 0x42000000, v234
	s_cbranch_scc1 .LBB0_347
.LBB0_337:
	s_cmpk_eq_i32 s20, 0xfec0
	s_cbranch_scc1 .LBB0_336
	s_add_i32 s0, s21, 31
	s_cmpk_gt_u32 s0, 0x81e
	s_cbranch_scc1 .LBB0_336
	ds_read_b128 v[198:201], v252
	ds_read_b128 v[194:197], v252 offset:32
	ds_read_b128 v[190:193], v252 offset:64
	ds_read_b128 v[186:189], v252 offset:96
	v_add_u32_e32 v235, s20, v246
	ds_read_b128 v[182:185], v235
	ds_read_b128 v[178:181], v235 offset:33280
	s_cmp_gt_u32 s19, 3
	s_mov_b64 s[0:1], -1
	s_cbranch_scc0 .LBB0_341
	v_fma_f32 v46, -v224, v234, -v249
	v_fmamk_f32 v32, v224, 0x80000000, v46
	v_sub_f32_e32 v33, v46, v224
	v_pk_fma_f32 v[34:35], v[226:227], s[28:29], v[46:47] op_sel_hi:[1,1,0]
	v_pk_fma_f32 v[36:37], v[226:227], s[84:85], v[46:47] op_sel_hi:[1,1,0]
	v_pk_fma_f32 v[38:39], v[226:227], s[82:83], v[46:47] op_sel_hi:[1,1,0]
	v_pk_fma_f32 v[40:41], v[226:227], s[26:27], v[46:47] op_sel_hi:[1,1,0]
	v_pk_fma_f32 v[42:43], v[226:227], s[24:25], v[46:47] op_sel_hi:[1,1,0]
	v_pk_fma_f32 v[44:45], v[226:227], s[86:87], v[46:47] op_sel_hi:[1,1,0]
	v_pk_fma_f32 v[46:47], v[226:227], s[2:3], v[46:47] op_sel_hi:[1,1,0]
	s_mov_b64 s[0:1], 0

.LBB0_345:
	s_waitcnt lgkmcnt(5)
	s_nop 0
	v_mfma_f32_32x32x16_bf16 v[32:47], v[198:201], v[50:53], v[32:47]
	s_waitcnt lgkmcnt(4)
	v_mfma_f32_32x32x16_bf16 v[32:47], v[194:197], v[54:57], v[32:47]
	s_waitcnt lgkmcnt(3)
	v_mfma_f32_32x32x16_bf16 v[32:47], v[190:193], v[58:61], v[32:47]
	s_waitcnt lgkmcnt(2)
	v_mfma_f32_32x32x16_bf16 v[32:47], v[186:189], v[62:65], v[32:47]
	ds_read_b128 v[190:193], v235 offset:32
	ds_read_b128 v[186:189], v235 offset:33312
	s_nop 9
	v_max3_f32 v194, v32, v33, v34
	v_max3_f32 v194, v194, v35, v36
	v_max3_f32 v194, v194, v37, v38
	v_max3_f32 v194, v194, v39, v40
	v_max3_f32 v194, v194, v41, v42
	v_max3_f32 v194, v194, v43, v44
	v_max3_f32 v194, v194, v45, v46
	v_max_f32_e32 v194, v194, v47
	v_cmp_lt_f32_e32 vcc, s84, v194
	s_cbranch_vccz .LBB0_335
	v_max_f32_e32 v194, v194, v194
	v_max_f32_e32 v194, 0, v194
	ds_bpermute_b32 v195, v243, v194
	s_waitcnt lgkmcnt(0)
	v_max_f32_e32 v195, v195, v195
	v_max_f32_e32 v194, v194, v195
	v_exp_f32_e64 v196, -v194
	v_pk_add_f32 v[32:33], v[32:33], v[194:195] op_sel_hi:[1,0] neg_lo:[0,1] neg_hi:[0,1]
	v_pk_add_f32 v[34:35], v[34:35], v[194:195] op_sel_hi:[1,0] neg_lo:[0,1] neg_hi:[0,1]
	v_pk_add_f32 v[36:37], v[36:37], v[194:195] op_sel_hi:[1,0] neg_lo:[0,1] neg_hi:[0,1]
	v_pk_add_f32 v[38:39], v[38:39], v[194:195] op_sel_hi:[1,0] neg_lo:[0,1] neg_hi:[0,1]
	v_pk_add_f32 v[40:41], v[40:41], v[194:195] op_sel_hi:[1,0] neg_lo:[0,1] neg_hi:[0,1]
	v_pk_add_f32 v[42:43], v[42:43], v[194:195] op_sel_hi:[1,0] neg_lo:[0,1] neg_hi:[0,1]
	v_pk_add_f32 v[44:45], v[44:45], v[194:195] op_sel_hi:[1,0] neg_lo:[0,1] neg_hi:[0,1]
	v_pk_add_f32 v[46:47], v[46:47], v[194:195] op_sel_hi:[1,0] neg_lo:[0,1] neg_hi:[0,1]
	v_pk_mul_f32 v[14:15], v[14:15], v[196:197] op_sel_hi:[1,0]
	v_pk_mul_f32 v[12:13], v[12:13], v[196:197] op_sel_hi:[1,0]
	v_pk_mul_f32 v[10:11], v[10:11], v[196:197] op_sel_hi:[1,0]
	v_pk_mul_f32 v[8:9], v[8:9], v[196:197] op_sel_hi:[1,0]
	v_pk_mul_f32 v[6:7], v[6:7], v[196:197] op_sel_hi:[1,0]
	v_pk_mul_f32 v[4:5], v[4:5], v[196:197] op_sel_hi:[1,0]
	v_pk_mul_f32 v[2:3], v[2:3], v[196:197] op_sel_hi:[1,0]
	v_pk_mul_f32 v[0:1], v[0:1], v[196:197] op_sel_hi:[1,0]
	v_pk_mul_f32 v[30:31], v[30:31], v[196:197] op_sel_hi:[1,0]
	v_pk_mul_f32 v[28:29], v[28:29], v[196:197] op_sel_hi:[1,0]
	v_pk_mul_f32 v[26:27], v[26:27], v[196:197] op_sel_hi:[1,0]
	v_pk_mul_f32 v[24:25], v[24:25], v[196:197] op_sel_hi:[1,0]
	v_pk_mul_f32 v[22:23], v[22:23], v[196:197] op_sel_hi:[1,0]
	v_pk_mul_f32 v[20:21], v[20:21], v[196:197] op_sel_hi:[1,0]
	v_pk_mul_f32 v[18:19], v[18:19], v[196:197] op_sel_hi:[1,0]
	v_pk_mul_f32 v[16:17], v[16:17], v[196:197] op_sel_hi:[1,0]
	v_mul_f32_e32 v250, v250, v196
	v_add_f32_e32 v249, v249, v194
	s_branch .LBB0_335

.LBB0_847:
	v_lshl_add_u32 v191, v188, 10, v6
	v_and_b32_e32 v6, 48, v4
	v_lshlrev_b32_e32 v7, 6, v4
	s_movk_i32 s13, 0x3c0
	s_add_u32 s58, s38, 0x1f100000
	v_and_or_b32 v6, v7, s13, v6
	v_lshlrev_b32_e32 v7, 2, v4
	s_addc_u32 s59, s39, 0
	s_lshl_b32 s12, s6, 6
	s_lshl_b32 s6, s6, 13
	v_and_b32_e32 v7, 32, v7
	v_bitop3_b32 v8, v6, s6, v7 bitop3:0xde
	s_lshl_b32 s6, s7, 5
	s_and_b32 s7, s6, 0x60
	s_lshl_b32 s6, s7, 7
	v_bitop3_b32 v192, s6, v6, v7 bitop3:0xf6
	s_sext_i32_i16 s6, s9
	s_lshl_b32 s6, s6, 3
	s_lshl_b32 s5, s5, 5
	s_add_i32 s5, s6, s5
	s_lshl_b32 s6, s10, 3
	s_sub_i32 s6, s8, s6
	s_sext_i32_i8 s6, s6
	s_add_i32 m0, s74, 0x18000
	v_lshl_add_u64 v[0:1], v[0:1], 0, s[88:89]
	s_add_i32 s6, s5, s6
	s_waitcnt vmcnt(2)
	s_barrier
	global_load_lds_dwordx4 v[0:1], off
	s_add_i32 m0, s74, 0x1a000
	s_add_u32 s60, s38, 0x7100080
	v_mov_b32_e32 v167, v49
	v_lshl_add_u64 v[0:1], v[2:3], 0, s[88:89]
	s_addc_u32 s61, s39, 0
	s_add_i32 s78, s74, 0x8000
	s_add_i32 s79, s74, 0xa000
	v_mov_b32_e32 v171, v49
	global_load_lds_dwordx4 v[0:1], off
	v_lshl_add_u64 v[0:1], s[60:61], 0, v[166:167]
	s_mov_b32 m0, s78
	s_add_u32 s8, s0, 0x20080
	global_load_lds_dwordx4 v[0:1], off
	v_lshl_add_u64 v[0:1], s[60:61], 0, v[170:171]
	s_mov_b32 m0, s79
	s_addc_u32 s9, s1, 0
	global_load_lds_dwordx4 v[0:1], off
	s_add_i32 m0, s74, 0x1c000
	v_lshl_add_u64 v[0:1], s[8:9], 0, v[162:163]
	global_load_lds_dwordx4 v[0:1], off
	v_lshl_add_u64 v[0:1], s[8:9], 0, v[164:165]
	s_add_i32 m0, s74, 0x1e000
	v_lshl_add_u32 v190, v186, 10, v5
	global_load_lds_dwordx4 v[0:1], off
	s_waitcnt vmcnt(6)
	v_lshrrev_b32_e32 v5, 1, v4
	s_cmpk_lt_u32 s4, 0x100
	s_cselect_b64 s[62:63], -1, 0
	v_and_or_b32 v167, v4, 31, s12
	v_and_or_b32 v171, v5, 16, s7
	s_mov_b32 s22, 0
	v_add_u32_e32 v193, 0, v8
	v_mov_b32_e32 v194, v191
	v_mov_b32_e32 v195, v190
	s_barrier
	v_mov_b32_e32 v32, 0
	v_mov_b32_e32 v33, 0
	v_mov_b32_e32 v34, 0
	v_mov_b32_e32 v35, 0
	v_mov_b32_e32 v36, 0
	v_mov_b32_e32 v37, 0
	v_mov_b32_e32 v38, 0
	v_mov_b32_e32 v39, 0
	v_mov_b32_e32 v40, 0
	v_mov_b32_e32 v41, 0
	v_mov_b32_e32 v42, 0
	v_mov_b32_e32 v43, 0
	v_mov_b32_e32 v44, 0
	v_mov_b32_e32 v45, 0
	v_mov_b32_e32 v46, 0
	v_mov_b32_e32 v47, 0
	v_mov_b32_e32 v50, 0
	v_mov_b32_e32 v51, 0
	v_mov_b32_e32 v52, 0
	v_mov_b32_e32 v53, 0
	v_mov_b32_e32 v54, 0
	v_mov_b32_e32 v55, 0
	v_mov_b32_e32 v56, 0
	v_mov_b32_e32 v57, 0
	v_mov_b32_e32 v58, 0
	v_mov_b32_e32 v59, 0
	v_mov_b32_e32 v60, 0
	v_mov_b32_e32 v61, 0
	v_mov_b32_e32 v62, 0
	v_mov_b32_e32 v63, 0
	v_mov_b32_e32 v64, 0
	v_mov_b32_e32 v65, 0
	v_mov_b32_e32 v66, 0
	v_mov_b32_e32 v67, 0
	v_mov_b32_e32 v68, 0
	v_mov_b32_e32 v69, 0
	v_mov_b32_e32 v70, 0
	v_mov_b32_e32 v71, 0
	v_mov_b32_e32 v72, 0
	v_mov_b32_e32 v73, 0
	v_mov_b32_e32 v74, 0
	v_mov_b32_e32 v75, 0
	v_mov_b32_e32 v76, 0
	v_mov_b32_e32 v77, 0
	v_mov_b32_e32 v78, 0
	v_mov_b32_e32 v79, 0
	v_mov_b32_e32 v80, 0
	v_mov_b32_e32 v81, 0
	v_mov_b32_e32 v82, 0
	v_mov_b32_e32 v83, 0
	v_mov_b32_e32 v84, 0
	v_mov_b32_e32 v85, 0
	v_mov_b32_e32 v86, 0
	v_mov_b32_e32 v87, 0
	v_mov_b32_e32 v88, 0
	v_mov_b32_e32 v89, 0
	v_mov_b32_e32 v90, 0
	v_mov_b32_e32 v91, 0
	v_mov_b32_e32 v92, 0
	v_mov_b32_e32 v93, 0
	v_mov_b32_e32 v94, 0
	v_mov_b32_e32 v95, 0
	v_mov_b32_e32 v96, 0
	v_mov_b32_e32 v97, 0
	v_mov_b32_e32 v98, 0
	v_mov_b32_e32 v99, 0
	v_mov_b32_e32 v100, 0
	v_mov_b32_e32 v101, 0
	v_mov_b32_e32 v102, 0
	v_mov_b32_e32 v103, 0
	v_mov_b32_e32 v104, 0
	v_mov_b32_e32 v105, 0
	v_mov_b32_e32 v106, 0
	v_mov_b32_e32 v107, 0
	v_mov_b32_e32 v108, 0
	v_mov_b32_e32 v109, 0
	v_mov_b32_e32 v110, 0
	v_mov_b32_e32 v111, 0
	v_mov_b32_e32 v112, 0
	v_mov_b32_e32 v113, 0
	v_mov_b32_e32 v114, 0
	v_mov_b32_e32 v115, 0
	v_mov_b32_e32 v116, 0
	v_mov_b32_e32 v117, 0
	v_mov_b32_e32 v118, 0
	v_mov_b32_e32 v119, 0
	v_mov_b32_e32 v120, 0
	v_mov_b32_e32 v121, 0
	v_mov_b32_e32 v122, 0
	v_mov_b32_e32 v123, 0
	v_mov_b32_e32 v124, 0
	v_mov_b32_e32 v125, 0
	v_mov_b32_e32 v126, 0
	v_mov_b32_e32 v127, 0
	v_mov_b32_e32 v128, 0
	v_mov_b32_e32 v129, 0
	v_mov_b32_e32 v130, 0
	v_mov_b32_e32 v131, 0
	v_mov_b32_e32 v132, 0
	v_mov_b32_e32 v133, 0
	v_mov_b32_e32 v134, 0
	v_mov_b32_e32 v135, 0
	v_mov_b32_e32 v136, 0
	v_mov_b32_e32 v137, 0
	v_mov_b32_e32 v138, 0
	v_mov_b32_e32 v139, 0
	v_mov_b32_e32 v140, 0
	v_mov_b32_e32 v141, 0
	v_mov_b32_e32 v142, 0
	v_mov_b32_e32 v143, 0
	v_mov_b32_e32 v144, 0
	v_mov_b32_e32 v145, 0
	v_mov_b32_e32 v146, 0
	v_mov_b32_e32 v147, 0
	v_mov_b32_e32 v148, 0
	v_mov_b32_e32 v149, 0
	v_mov_b32_e32 v150, 0
	v_mov_b32_e32 v151, 0
	v_mov_b32_e32 v152, 0
	v_mov_b32_e32 v153, 0
	v_mov_b32_e32 v154, 0
	v_mov_b32_e32 v155, 0
	v_mov_b32_e32 v156, 0
	v_mov_b32_e32 v157, 0
	v_mov_b32_e32 v158, 0
	v_mov_b32_e32 v159, 0
	v_mov_b32_e32 v160, 0
	v_mov_b32_e32 v161, 0
	s_branch .LBB0_850

.LBB0_856:
	s_ashr_i32 s65, s64, 31
	s_lshl_b64 s[8:9], s[64:65], 18
	s_add_u32 s66, s72, s8
	s_addc_u32 s67, s73, s9
	s_and_b64 s[8:9], s[38:39], exec
	s_cselect_b32 s4, s67, s1
	s_cselect_b32 s7, s66, s0
	s_lshl_b32 s8, s22, 10
	s_add_i32 s8, s8, 0
	s_add_i32 s8, s8, 0x20000
	v_lshl_add_u32 v196, v186, 2, s8
	v_lshl_add_u32 v197, v188, 2, s8
	s_add_u32 s8, s0, 0x100
	v_mov_b32_e32 v169, v49
	v_mov_b32_e32 v173, v49
	s_addc_u32 s9, s1, 0
	s_mov_b32 s10, -2
	s_mov_b64 s[70:71], s[60:61]
	s_branch .LBB0_858

.LBB0_862:
	s_lshl_b32 s0, s68, 7
	s_mov_b32 s69, 0x48000000
	v_lshl_add_u32 v6, s6, 8, v167
	s_and_b32 s0, s0, 0x380
	v_or_b32_e32 v48, s0, v171
	s_nop 15
	s_nop 15
	s_mov_b32 s0, 0x20000
	v_mul_f32_e32 v24, 0xbab8aa3b, v158
	v_mul_f32_e32 v25, 0xbab8aa3b, v159
	v_mul_f32_e32 v26, 0xbab8aa3b, v160
	v_mul_f32_e32 v27, 0xbab8aa3b, v161
	v_mul_f32_e32 v28, 0xbab8aa3b, v150
	v_mul_f32_e32 v29, 0xbab8aa3b, v151
	v_mul_f32_e32 v30, 0xbab8aa3b, v152
	v_mul_f32_e32 v31, 0xbab8aa3b, v153
	v_min_f32_e32 v24, 0x42200000, v24
	v_min_f32_e32 v25, 0x42200000, v25
	v_min_f32_e32 v26, 0x42200000, v26
	v_min_f32_e32 v27, 0x42200000, v27
	v_min_f32_e32 v28, 0x42200000, v28
	v_min_f32_e32 v29, 0x42200000, v29
	v_min_f32_e32 v30, 0x42200000, v30
	v_min_f32_e32 v31, 0x42200000, v31
	v_exp_f32_e32 v24, v24
	v_exp_f32_e32 v25, v25
	v_exp_f32_e32 v26, v26
	v_exp_f32_e32 v27, v27
	v_exp_f32_e32 v28, v28
	v_exp_f32_e32 v29, v29
	v_exp_f32_e32 v30, v30
	v_exp_f32_e32 v31, v31
	v_mul_f32_e32 v8, v158, v154
	v_mul_f32_e32 v9, v159, v155
	v_mul_f32_e32 v10, v160, v156
	v_mul_f32_e32 v11, v161, v157
	v_mul_f32_e32 v12, v150, v146
	v_mul_f32_e32 v13, v151, v147
	v_mul_f32_e32 v14, v152, v148
	v_mul_f32_e32 v15, v153, v149
	v_fma_f32 v24, v24, s69, s69
	v_fma_f32 v25, v25, s69, s69
	v_fma_f32 v26, v26, s69, s69
	v_fma_f32 v27, v27, s69, s69
	v_fma_f32 v28, v28, s69, s69
	v_fma_f32 v29, v29, s69, s69
	v_fma_f32 v30, v30, s69, s69
	v_fma_f32 v31, v31, s69, s69
	v_mul_f32_e32 v0, v24, v25
	v_mul_f32_e32 v1, v26, v27
	v_mul_f32_e32 v2, v28, v29
	v_mul_f32_e32 v3, v30, v31
	v_rcp_f32_e32 v0, v0
	v_rcp_f32_e32 v1, v1
	v_rcp_f32_e32 v2, v2
	v_rcp_f32_e32 v3, v3
	v_mul_f32_e32 v8, v8, v25
	v_mul_f32_e32 v10, v10, v27
	v_mul_f32_e32 v12, v12, v29
	v_mul_f32_e32 v14, v14, v31
	v_mul_f32_e32 v9, v9, v24
	v_mul_f32_e32 v11, v11, v26
	v_mul_f32_e32 v13, v13, v28
	v_mul_f32_e32 v15, v15, v30
	v_mul_f32_e32 v8, v8, v0
	v_mul_f32_e32 v9, v9, v0
	v_mul_f32_e32 v10, v10, v1
	v_mul_f32_e32 v11, v11, v1
	v_mul_f32_e32 v12, v12, v2
	v_mul_f32_e32 v13, v13, v2
	v_mul_f32_e32 v14, v14, v3
	v_mul_f32_e32 v15, v15, v3
	v_med3_f32 v8, v8, s11, v232
	v_med3_f32 v9, v9, s11, v232
	v_med3_f32 v10, v10, s11, v232
	v_med3_f32 v11, v11, s11, v232
	v_med3_f32 v12, v12, s11, v232
	v_med3_f32 v13, v13, s11, v232
	v_med3_f32 v14, v14, s11, v232
	v_med3_f32 v15, v15, s11, v232
	v_mul_f32_e32 v24, 0xbab8aa3b, v142
	v_mul_f32_e32 v25, 0xbab8aa3b, v143
	v_mul_f32_e32 v26, 0xbab8aa3b, v144
	v_mul_f32_e32 v27, 0xbab8aa3b, v145
	v_mul_f32_e32 v28, 0xbab8aa3b, v134
	v_mul_f32_e32 v29, 0xbab8aa3b, v135
	v_mul_f32_e32 v30, 0xbab8aa3b, v136
	v_mul_f32_e32 v31, 0xbab8aa3b, v137
	v_min_f32_e32 v24, 0x42200000, v24
	v_min_f32_e32 v25, 0x42200000, v25
	v_min_f32_e32 v26, 0x42200000, v26
	v_min_f32_e32 v27, 0x42200000, v27
	v_min_f32_e32 v28, 0x42200000, v28
	v_min_f32_e32 v29, 0x42200000, v29
	v_min_f32_e32 v30, 0x42200000, v30
	v_min_f32_e32 v31, 0x42200000, v31
	v_exp_f32_e32 v24, v24
	v_exp_f32_e32 v25, v25
	v_exp_f32_e32 v26, v26
	v_exp_f32_e32 v27, v27
	v_exp_f32_e32 v28, v28
	v_exp_f32_e32 v29, v29
	v_exp_f32_e32 v30, v30
	v_exp_f32_e32 v31, v31
	v_mul_f32_e32 v16, v142, v138
	v_mul_f32_e32 v17, v143, v139
	v_mul_f32_e32 v18, v144, v140
	v_mul_f32_e32 v19, v145, v141
	v_mul_f32_e32 v20, v134, v130
	v_mul_f32_e32 v21, v135, v131
	v_mul_f32_e32 v22, v136, v132
	v_mul_f32_e32 v23, v137, v133
	v_fma_f32 v24, v24, s69, s69
	v_fma_f32 v25, v25, s69, s69
	v_fma_f32 v26, v26, s69, s69
	v_fma_f32 v27, v27, s69, s69
	v_fma_f32 v28, v28, s69, s69
	v_fma_f32 v29, v29, s69, s69
	v_fma_f32 v30, v30, s69, s69
	v_fma_f32 v31, v31, s69, s69
	v_mul_f32_e32 v0, v24, v25
	v_mul_f32_e32 v1, v26, v27
	v_mul_f32_e32 v2, v28, v29
	v_mul_f32_e32 v3, v30, v31
	v_rcp_f32_e32 v0, v0
	v_rcp_f32_e32 v1, v1
	v_rcp_f32_e32 v2, v2
	v_rcp_f32_e32 v3, v3
	v_mul_f32_e32 v16, v16, v25
	v_mul_f32_e32 v18, v18, v27
	v_mul_f32_e32 v20, v20, v29
	v_mul_f32_e32 v22, v22, v31
	v_mul_f32_e32 v17, v17, v24
	v_mul_f32_e32 v19, v19, v26
	v_mul_f32_e32 v21, v21, v28
	v_mul_f32_e32 v23, v23, v30
	v_mul_f32_e32 v16, v16, v0
	v_mul_f32_e32 v17, v17, v0
	v_mul_f32_e32 v18, v18, v1
	v_mul_f32_e32 v19, v19, v1
	v_mul_f32_e32 v20, v20, v2
	v_mul_f32_e32 v21, v21, v2
	v_mul_f32_e32 v22, v22, v3
	v_mul_f32_e32 v23, v23, v3
	v_med3_f32 v16, v16, s11, v232
	v_med3_f32 v17, v17, s11, v232
	v_med3_f32 v18, v18, s11, v232
	v_med3_f32 v19, v19, s11, v232
	v_med3_f32 v20, v20, s11, v232
	v_med3_f32 v21, v21, s11, v232
	v_med3_f32 v22, v22, s11, v232
	v_med3_f32 v23, v23, s11, v232
	v_cvt_pk_fp8_f32 v0, v8, v9
	v_cvt_pk_fp8_f32 v1, v12, v13
	v_cvt_pk_fp8_f32 v2, v16, v17
	v_cvt_pk_fp8_f32 v3, v20, v21
	v_cvt_pk_fp8_f32 v0, v10, v11 op_sel:[0,0,1]
	v_cvt_pk_fp8_f32 v1, v14, v15 op_sel:[0,0,1]
	v_cvt_pk_fp8_f32 v2, v18, v19 op_sel:[0,0,1]
	v_cvt_pk_fp8_f32 v3, v22, v23 op_sel:[0,0,1]
	v_ashrrev_i32_e32 v7, 31, v6
	v_lshlrev_b64 v[4:5], 10, v[6:7]
	v_lshl_add_u64 v[4:5], s[58:59], 0, v[4:5]
	v_lshl_add_u64 v[4:5], v[4:5], 0, v[48:49]
	s_nop 1
	v_permlane16_swap_b32_e32 v0, v2
	v_permlane16_swap_b32_e32 v1, v3
	global_store_dwordx4 v[4:5], v[0:3], off
	v_mov_b32_e32 v130, 0
	v_mov_b32_e32 v131, 0
	v_mov_b32_e32 v132, 0
	v_mov_b32_e32 v133, 0
	v_mov_b32_e32 v134, 0
	v_mov_b32_e32 v135, 0
	v_mov_b32_e32 v136, 0
	v_mov_b32_e32 v137, 0
	v_mov_b32_e32 v138, 0
	v_mov_b32_e32 v139, 0
	v_mov_b32_e32 v140, 0
	v_mov_b32_e32 v141, 0
	v_mov_b32_e32 v142, 0
	v_mov_b32_e32 v143, 0
	v_mov_b32_e32 v144, 0
	v_mov_b32_e32 v145, 0
	v_mov_b32_e32 v146, 0
	v_mov_b32_e32 v147, 0
	v_mov_b32_e32 v148, 0
	v_mov_b32_e32 v149, 0
	v_mov_b32_e32 v150, 0
	v_mov_b32_e32 v151, 0
	v_mov_b32_e32 v152, 0
	v_mov_b32_e32 v153, 0
	v_mov_b32_e32 v154, 0
	v_mov_b32_e32 v155, 0
	v_mov_b32_e32 v156, 0
	v_mov_b32_e32 v157, 0
	v_mov_b32_e32 v158, 0
	v_mov_b32_e32 v159, 0
	v_mov_b32_e32 v160, 0
	v_mov_b32_e32 v161, 0
	v_or_b32_e32 v6, 32, v6
	v_mul_f32_e32 v24, 0xbab8aa3b, v126
	v_mul_f32_e32 v25, 0xbab8aa3b, v127
	v_mul_f32_e32 v26, 0xbab8aa3b, v128
	v_mul_f32_e32 v27, 0xbab8aa3b, v129
	v_mul_f32_e32 v28, 0xbab8aa3b, v118
	v_mul_f32_e32 v29, 0xbab8aa3b, v119
	v_mul_f32_e32 v30, 0xbab8aa3b, v120
	v_mul_f32_e32 v31, 0xbab8aa3b, v121
	v_min_f32_e32 v24, 0x42200000, v24
	v_min_f32_e32 v25, 0x42200000, v25
	v_min_f32_e32 v26, 0x42200000, v26
	v_min_f32_e32 v27, 0x42200000, v27
	v_min_f32_e32 v28, 0x42200000, v28
	v_min_f32_e32 v29, 0x42200000, v29
	v_min_f32_e32 v30, 0x42200000, v30
	v_min_f32_e32 v31, 0x42200000, v31
	v_exp_f32_e32 v24, v24
	v_exp_f32_e32 v25, v25
	v_exp_f32_e32 v26, v26
	v_exp_f32_e32 v27, v27
	v_exp_f32_e32 v28, v28
	v_exp_f32_e32 v29, v29
	v_exp_f32_e32 v30, v30
	v_exp_f32_e32 v31, v31
	v_mul_f32_e32 v8, v126, v122
	v_mul_f32_e32 v9, v127, v123
	v_mul_f32_e32 v10, v128, v124
	v_mul_f32_e32 v11, v129, v125
	v_mul_f32_e32 v12, v118, v114
	v_mul_f32_e32 v13, v119, v115
	v_mul_f32_e32 v14, v120, v116
	v_mul_f32_e32 v15, v121, v117
	v_fma_f32 v24, v24, s69, s69
	v_fma_f32 v25, v25, s69, s69
	v_fma_f32 v26, v26, s69, s69
	v_fma_f32 v27, v27, s69, s69
	v_fma_f32 v28, v28, s69, s69
	v_fma_f32 v29, v29, s69, s69
	v_fma_f32 v30, v30, s69, s69
	v_fma_f32 v31, v31, s69, s69
	v_mul_f32_e32 v0, v24, v25
	v_mul_f32_e32 v1, v26, v27
	v_mul_f32_e32 v2, v28, v29
	v_mul_f32_e32 v3, v30, v31
	v_rcp_f32_e32 v0, v0
	v_rcp_f32_e32 v1, v1
	v_rcp_f32_e32 v2, v2
	v_rcp_f32_e32 v3, v3
	v_mul_f32_e32 v8, v8, v25
	v_mul_f32_e32 v10, v10, v27
	v_mul_f32_e32 v12, v12, v29
	v_mul_f32_e32 v14, v14, v31
	v_mul_f32_e32 v9, v9, v24
	v_mul_f32_e32 v11, v11, v26
	v_mul_f32_e32 v13, v13, v28
	v_mul_f32_e32 v15, v15, v30
	v_mul_f32_e32 v8, v8, v0
	v_mul_f32_e32 v9, v9, v0
	v_mul_f32_e32 v10, v10, v1
	v_mul_f32_e32 v11, v11, v1
	v_mul_f32_e32 v12, v12, v2
	v_mul_f32_e32 v13, v13, v2
	v_mul_f32_e32 v14, v14, v3
	v_mul_f32_e32 v15, v15, v3
	v_med3_f32 v8, v8, s11, v232
	v_med3_f32 v9, v9, s11, v232
	v_med3_f32 v10, v10, s11, v232
	v_med3_f32 v11, v11, s11, v232
	v_med3_f32 v12, v12, s11, v232
	v_med3_f32 v13, v13, s11, v232
	v_med3_f32 v14, v14, s11, v232
	v_med3_f32 v15, v15, s11, v232
	v_mul_f32_e32 v24, 0xbab8aa3b, v110
	v_mul_f32_e32 v25, 0xbab8aa3b, v111
	v_mul_f32_e32 v26, 0xbab8aa3b, v112
	v_mul_f32_e32 v27, 0xbab8aa3b, v113
	v_mul_f32_e32 v28, 0xbab8aa3b, v102
	v_mul_f32_e32 v29, 0xbab8aa3b, v103
	v_mul_f32_e32 v30, 0xbab8aa3b, v104
	v_mul_f32_e32 v31, 0xbab8aa3b, v105
	v_min_f32_e32 v24, 0x42200000, v24
	v_min_f32_e32 v25, 0x42200000, v25
	v_min_f32_e32 v26, 0x42200000, v26
	v_min_f32_e32 v27, 0x42200000, v27
	v_min_f32_e32 v28, 0x42200000, v28
	v_min_f32_e32 v29, 0x42200000, v29
	v_min_f32_e32 v30, 0x42200000, v30
	v_min_f32_e32 v31, 0x42200000, v31
	v_exp_f32_e32 v24, v24
	v_exp_f32_e32 v25, v25
	v_exp_f32_e32 v26, v26
	v_exp_f32_e32 v27, v27
	v_exp_f32_e32 v28, v28
	v_exp_f32_e32 v29, v29
	v_exp_f32_e32 v30, v30
	v_exp_f32_e32 v31, v31
	v_mul_f32_e32 v16, v110, v106
	v_mul_f32_e32 v17, v111, v107
	v_mul_f32_e32 v18, v112, v108
	v_mul_f32_e32 v19, v113, v109
	v_mul_f32_e32 v20, v102, v98
	v_mul_f32_e32 v21, v103, v99
	v_mul_f32_e32 v22, v104, v100
	v_mul_f32_e32 v23, v105, v101
	v_fma_f32 v24, v24, s69, s69
	v_fma_f32 v25, v25, s69, s69
	v_fma_f32 v26, v26, s69, s69
	v_fma_f32 v27, v27, s69, s69
	v_fma_f32 v28, v28, s69, s69
	v_fma_f32 v29, v29, s69, s69
	v_fma_f32 v30, v30, s69, s69
	v_fma_f32 v31, v31, s69, s69
	v_mul_f32_e32 v0, v24, v25
	v_mul_f32_e32 v1, v26, v27
	v_mul_f32_e32 v2, v28, v29
	v_mul_f32_e32 v3, v30, v31
	v_rcp_f32_e32 v0, v0
	v_rcp_f32_e32 v1, v1
	v_rcp_f32_e32 v2, v2
	v_rcp_f32_e32 v3, v3
	v_mul_f32_e32 v16, v16, v25
	v_mul_f32_e32 v18, v18, v27
	v_mul_f32_e32 v20, v20, v29
	v_mul_f32_e32 v22, v22, v31
	v_mul_f32_e32 v17, v17, v24
	v_mul_f32_e32 v19, v19, v26
	v_mul_f32_e32 v21, v21, v28
	v_mul_f32_e32 v23, v23, v30
	v_mul_f32_e32 v16, v16, v0
	v_mul_f32_e32 v17, v17, v0
	v_mul_f32_e32 v18, v18, v1
	v_mul_f32_e32 v19, v19, v1
	v_mul_f32_e32 v20, v20, v2
	v_mul_f32_e32 v21, v21, v2
	v_mul_f32_e32 v22, v22, v3
	v_mul_f32_e32 v23, v23, v3
	v_med3_f32 v16, v16, s11, v232
	v_med3_f32 v17, v17, s11, v232
	v_med3_f32 v18, v18, s11, v232
	v_med3_f32 v19, v19, s11, v232
	v_med3_f32 v20, v20, s11, v232
	v_med3_f32 v21, v21, s11, v232
	v_med3_f32 v22, v22, s11, v232
	v_med3_f32 v23, v23, s11, v232
	v_cvt_pk_fp8_f32 v0, v8, v9
	v_cvt_pk_fp8_f32 v1, v12, v13
	v_cvt_pk_fp8_f32 v2, v16, v17
	v_cvt_pk_fp8_f32 v3, v20, v21
	v_cvt_pk_fp8_f32 v0, v10, v11 op_sel:[0,0,1]
	v_cvt_pk_fp8_f32 v1, v14, v15 op_sel:[0,0,1]
	v_cvt_pk_fp8_f32 v2, v18, v19 op_sel:[0,0,1]
	v_cvt_pk_fp8_f32 v3, v22, v23 op_sel:[0,0,1]
	v_ashrrev_i32_e32 v7, 31, v6
	v_lshlrev_b64 v[6:7], 10, v[6:7]
	v_lshl_add_u64 v[6:7], s[58:59], 0, v[6:7]
	v_lshl_add_u64 v[6:7], v[6:7], 0, v[48:49]
	s_nop 1
	v_permlane16_swap_b32_e32 v0, v2
	v_permlane16_swap_b32_e32 v1, v3
	global_store_dwordx4 v[6:7], v[0:3], off
	v_mov_b32_e32 v98, 0
	v_mov_b32_e32 v99, 0
	v_mov_b32_e32 v100, 0
	v_mov_b32_e32 v101, 0
	v_mov_b32_e32 v102, 0
	v_mov_b32_e32 v103, 0
	v_mov_b32_e32 v104, 0
	v_mov_b32_e32 v105, 0
	v_mov_b32_e32 v106, 0
	v_mov_b32_e32 v107, 0
	v_mov_b32_e32 v108, 0
	v_mov_b32_e32 v109, 0
	v_mov_b32_e32 v110, 0
	v_mov_b32_e32 v111, 0
	v_mov_b32_e32 v112, 0
	v_mov_b32_e32 v113, 0
	v_mov_b32_e32 v114, 0
	v_mov_b32_e32 v115, 0
	v_mov_b32_e32 v116, 0
	v_mov_b32_e32 v117, 0
	v_mov_b32_e32 v118, 0
	v_mov_b32_e32 v119, 0
	v_mov_b32_e32 v120, 0
	v_mov_b32_e32 v121, 0
	v_mov_b32_e32 v122, 0
	v_mov_b32_e32 v123, 0
	v_mov_b32_e32 v124, 0
	v_mov_b32_e32 v125, 0
	v_mov_b32_e32 v126, 0
	v_mov_b32_e32 v127, 0
	v_mov_b32_e32 v128, 0
	v_mov_b32_e32 v129, 0
	v_mul_f32_e32 v24, 0xbab8aa3b, v94
	v_mul_f32_e32 v25, 0xbab8aa3b, v95
	v_mul_f32_e32 v26, 0xbab8aa3b, v96
	v_mul_f32_e32 v27, 0xbab8aa3b, v97
	v_mul_f32_e32 v28, 0xbab8aa3b, v86
	v_mul_f32_e32 v29, 0xbab8aa3b, v87
	v_mul_f32_e32 v30, 0xbab8aa3b, v88
	v_mul_f32_e32 v31, 0xbab8aa3b, v89
	v_min_f32_e32 v24, 0x42200000, v24
	v_min_f32_e32 v25, 0x42200000, v25
	v_min_f32_e32 v26, 0x42200000, v26
	v_min_f32_e32 v27, 0x42200000, v27
	v_min_f32_e32 v28, 0x42200000, v28
	v_min_f32_e32 v29, 0x42200000, v29
	v_min_f32_e32 v30, 0x42200000, v30
	v_min_f32_e32 v31, 0x42200000, v31
	v_exp_f32_e32 v24, v24
	v_exp_f32_e32 v25, v25
	v_exp_f32_e32 v26, v26
	v_exp_f32_e32 v27, v27
	v_exp_f32_e32 v28, v28
	v_exp_f32_e32 v29, v29
	v_exp_f32_e32 v30, v30
	v_exp_f32_e32 v31, v31
	v_mul_f32_e32 v8, v94, v90
	v_mul_f32_e32 v9, v95, v91
	v_mul_f32_e32 v10, v96, v92
	v_mul_f32_e32 v11, v97, v93
	v_mul_f32_e32 v12, v86, v82
	v_mul_f32_e32 v13, v87, v83
	v_mul_f32_e32 v14, v88, v84
	v_mul_f32_e32 v15, v89, v85
	v_fma_f32 v24, v24, s69, s69
	v_fma_f32 v25, v25, s69, s69
	v_fma_f32 v26, v26, s69, s69
	v_fma_f32 v27, v27, s69, s69
	v_fma_f32 v28, v28, s69, s69
	v_fma_f32 v29, v29, s69, s69
	v_fma_f32 v30, v30, s69, s69
	v_fma_f32 v31, v31, s69, s69
	v_mul_f32_e32 v0, v24, v25
	v_mul_f32_e32 v1, v26, v27
	v_mul_f32_e32 v2, v28, v29
	v_mul_f32_e32 v3, v30, v31
	v_rcp_f32_e32 v0, v0
	v_rcp_f32_e32 v1, v1
	v_rcp_f32_e32 v2, v2
	v_rcp_f32_e32 v3, v3
	v_mul_f32_e32 v8, v8, v25
	v_mul_f32_e32 v10, v10, v27
	v_mul_f32_e32 v12, v12, v29
	v_mul_f32_e32 v14, v14, v31
	v_mul_f32_e32 v9, v9, v24
	v_mul_f32_e32 v11, v11, v26
	v_mul_f32_e32 v13, v13, v28
	v_mul_f32_e32 v15, v15, v30
	v_mul_f32_e32 v8, v8, v0
	v_mul_f32_e32 v9, v9, v0
	v_mul_f32_e32 v10, v10, v1
	v_mul_f32_e32 v11, v11, v1
	v_mul_f32_e32 v12, v12, v2
	v_mul_f32_e32 v13, v13, v2
	v_mul_f32_e32 v14, v14, v3
	v_mul_f32_e32 v15, v15, v3
	v_med3_f32 v8, v8, s11, v232
	v_med3_f32 v9, v9, s11, v232
	v_med3_f32 v10, v10, s11, v232
	v_med3_f32 v11, v11, s11, v232
	v_med3_f32 v12, v12, s11, v232
	v_med3_f32 v13, v13, s11, v232
	v_med3_f32 v14, v14, s11, v232
	v_med3_f32 v15, v15, s11, v232
	v_mul_f32_e32 v24, 0xbab8aa3b, v78
	v_mul_f32_e32 v25, 0xbab8aa3b, v79
	v_mul_f32_e32 v26, 0xbab8aa3b, v80
	v_mul_f32_e32 v27, 0xbab8aa3b, v81
	v_mul_f32_e32 v28, 0xbab8aa3b, v70
	v_mul_f32_e32 v29, 0xbab8aa3b, v71
	v_mul_f32_e32 v30, 0xbab8aa3b, v72
	v_mul_f32_e32 v31, 0xbab8aa3b, v73
	v_min_f32_e32 v24, 0x42200000, v24
	v_min_f32_e32 v25, 0x42200000, v25
	v_min_f32_e32 v26, 0x42200000, v26
	v_min_f32_e32 v27, 0x42200000, v27
	v_min_f32_e32 v28, 0x42200000, v28
	v_min_f32_e32 v29, 0x42200000, v29
	v_min_f32_e32 v30, 0x42200000, v30
	v_min_f32_e32 v31, 0x42200000, v31
	v_exp_f32_e32 v24, v24
	v_exp_f32_e32 v25, v25
	v_exp_f32_e32 v26, v26
	v_exp_f32_e32 v27, v27
	v_exp_f32_e32 v28, v28
	v_exp_f32_e32 v29, v29
	v_exp_f32_e32 v30, v30
	v_exp_f32_e32 v31, v31
	v_mul_f32_e32 v16, v78, v74
	v_mul_f32_e32 v17, v79, v75
	v_mul_f32_e32 v18, v80, v76
	v_mul_f32_e32 v19, v81, v77
	v_mul_f32_e32 v20, v70, v66
	v_mul_f32_e32 v21, v71, v67
	v_mul_f32_e32 v22, v72, v68
	v_mul_f32_e32 v23, v73, v69
	v_fma_f32 v24, v24, s69, s69
	v_fma_f32 v25, v25, s69, s69
	v_fma_f32 v26, v26, s69, s69
	v_fma_f32 v27, v27, s69, s69
	v_fma_f32 v28, v28, s69, s69
	v_fma_f32 v29, v29, s69, s69
	v_fma_f32 v30, v30, s69, s69
	v_fma_f32 v31, v31, s69, s69
	v_mul_f32_e32 v0, v24, v25
	v_mul_f32_e32 v1, v26, v27
	v_mul_f32_e32 v2, v28, v29
	v_mul_f32_e32 v3, v30, v31
	v_rcp_f32_e32 v0, v0
	v_rcp_f32_e32 v1, v1
	v_rcp_f32_e32 v2, v2
	v_rcp_f32_e32 v3, v3
	v_mul_f32_e32 v16, v16, v25
	v_mul_f32_e32 v18, v18, v27
	v_mul_f32_e32 v20, v20, v29
	v_mul_f32_e32 v22, v22, v31
	v_mul_f32_e32 v17, v17, v24
	v_mul_f32_e32 v19, v19, v26
	v_mul_f32_e32 v21, v21, v28
	v_mul_f32_e32 v23, v23, v30
	v_mul_f32_e32 v16, v16, v0
	v_mul_f32_e32 v17, v17, v0
	v_mul_f32_e32 v18, v18, v1
	v_mul_f32_e32 v19, v19, v1
	v_mul_f32_e32 v20, v20, v2
	v_mul_f32_e32 v21, v21, v2
	v_mul_f32_e32 v22, v22, v3
	v_mul_f32_e32 v23, v23, v3
	v_med3_f32 v16, v16, s11, v232
	v_med3_f32 v17, v17, s11, v232
	v_med3_f32 v18, v18, s11, v232
	v_med3_f32 v19, v19, s11, v232
	v_med3_f32 v20, v20, s11, v232
	v_med3_f32 v21, v21, s11, v232
	v_med3_f32 v22, v22, s11, v232
	v_med3_f32 v23, v23, s11, v232
	v_cvt_pk_fp8_f32 v0, v8, v9
	v_cvt_pk_fp8_f32 v1, v12, v13
	v_cvt_pk_fp8_f32 v2, v16, v17
	v_cvt_pk_fp8_f32 v3, v20, v21
	v_cvt_pk_fp8_f32 v0, v10, v11 op_sel:[0,0,1]
	v_cvt_pk_fp8_f32 v1, v14, v15 op_sel:[0,0,1]
	v_cvt_pk_fp8_f32 v2, v18, v19 op_sel:[0,0,1]
	v_cvt_pk_fp8_f32 v3, v22, v23 op_sel:[0,0,1]
	v_add_co_u32_e32 v6, vcc, s0, v4
	s_nop 1
	v_addc_co_u32_e32 v7, vcc, 0, v5, vcc
	s_nop 1
	v_permlane16_swap_b32_e32 v0, v2
	v_permlane16_swap_b32_e32 v1, v3
	global_store_dwordx4 v[6:7], v[0:3], off
	v_mov_b32_e32 v66, 0
	v_mov_b32_e32 v67, 0
	v_mov_b32_e32 v68, 0
	v_mov_b32_e32 v69, 0
	v_mov_b32_e32 v70, 0
	v_mov_b32_e32 v71, 0
	v_mov_b32_e32 v72, 0
	v_mov_b32_e32 v73, 0
	v_mov_b32_e32 v74, 0
	v_mov_b32_e32 v75, 0
	v_mov_b32_e32 v76, 0
	v_mov_b32_e32 v77, 0
	v_mov_b32_e32 v78, 0
	v_mov_b32_e32 v79, 0
	v_mov_b32_e32 v80, 0
	v_mov_b32_e32 v81, 0
	v_mov_b32_e32 v82, 0
	v_mov_b32_e32 v83, 0
	v_mov_b32_e32 v84, 0
	v_mov_b32_e32 v85, 0
	v_mov_b32_e32 v86, 0
	v_mov_b32_e32 v87, 0
	v_mov_b32_e32 v88, 0
	v_mov_b32_e32 v89, 0
	v_mov_b32_e32 v90, 0
	v_mov_b32_e32 v91, 0
	v_mov_b32_e32 v92, 0
	v_mov_b32_e32 v93, 0
	v_mov_b32_e32 v94, 0
	v_mov_b32_e32 v95, 0
	v_mov_b32_e32 v96, 0
	v_mov_b32_e32 v97, 0
	v_mul_f32_e32 v24, 0xbab8aa3b, v62
	v_mul_f32_e32 v25, 0xbab8aa3b, v63
	v_mul_f32_e32 v26, 0xbab8aa3b, v64
	v_mul_f32_e32 v27, 0xbab8aa3b, v65
	v_mul_f32_e32 v28, 0xbab8aa3b, v54
	v_mul_f32_e32 v29, 0xbab8aa3b, v55
	v_mul_f32_e32 v30, 0xbab8aa3b, v56
	v_mul_f32_e32 v31, 0xbab8aa3b, v57
	v_min_f32_e32 v24, 0x42200000, v24
	v_min_f32_e32 v25, 0x42200000, v25
	v_min_f32_e32 v26, 0x42200000, v26
	v_min_f32_e32 v27, 0x42200000, v27
	v_min_f32_e32 v28, 0x42200000, v28
	v_min_f32_e32 v29, 0x42200000, v29
	v_min_f32_e32 v30, 0x42200000, v30
	v_min_f32_e32 v31, 0x42200000, v31
	v_exp_f32_e32 v24, v24
	v_exp_f32_e32 v25, v25
	v_exp_f32_e32 v26, v26
	v_exp_f32_e32 v27, v27
	v_exp_f32_e32 v28, v28
	v_exp_f32_e32 v29, v29
	v_exp_f32_e32 v30, v30
	v_exp_f32_e32 v31, v31
	v_mul_f32_e32 v8, v62, v58
	v_mul_f32_e32 v9, v63, v59
	v_mul_f32_e32 v10, v64, v60
	v_mul_f32_e32 v11, v65, v61
	v_mul_f32_e32 v12, v54, v50
	v_mul_f32_e32 v13, v55, v51
	v_mul_f32_e32 v14, v56, v52
	v_mul_f32_e32 v15, v57, v53
	v_fma_f32 v24, v24, s69, s69
	v_fma_f32 v25, v25, s69, s69
	v_fma_f32 v26, v26, s69, s69
	v_fma_f32 v27, v27, s69, s69
	v_fma_f32 v28, v28, s69, s69
	v_fma_f32 v29, v29, s69, s69
	v_fma_f32 v30, v30, s69, s69
	v_fma_f32 v31, v31, s69, s69
	v_mul_f32_e32 v0, v24, v25
	v_mul_f32_e32 v1, v26, v27
	v_mul_f32_e32 v2, v28, v29
	v_mul_f32_e32 v3, v30, v31
	v_rcp_f32_e32 v0, v0
	v_rcp_f32_e32 v1, v1
	v_rcp_f32_e32 v2, v2
	v_rcp_f32_e32 v3, v3
	v_mul_f32_e32 v8, v8, v25
	v_mul_f32_e32 v10, v10, v27
	v_mul_f32_e32 v12, v12, v29
	v_mul_f32_e32 v14, v14, v31
	v_mul_f32_e32 v9, v9, v24
	v_mul_f32_e32 v11, v11, v26
	v_mul_f32_e32 v13, v13, v28
	v_mul_f32_e32 v15, v15, v30
	v_mul_f32_e32 v8, v8, v0
	v_mul_f32_e32 v9, v9, v0
	v_mul_f32_e32 v10, v10, v1
	v_mul_f32_e32 v11, v11, v1
	v_mul_f32_e32 v12, v12, v2
	v_mul_f32_e32 v13, v13, v2
	v_mul_f32_e32 v14, v14, v3
	v_mul_f32_e32 v15, v15, v3
	v_med3_f32 v8, v8, s11, v232
	v_med3_f32 v9, v9, s11, v232
	v_med3_f32 v10, v10, s11, v232
	v_med3_f32 v11, v11, s11, v232
	v_med3_f32 v12, v12, s11, v232
	v_med3_f32 v13, v13, s11, v232
	v_med3_f32 v14, v14, s11, v232
	v_med3_f32 v15, v15, s11, v232
	v_mul_f32_e32 v24, 0xbab8aa3b, v44
	v_mul_f32_e32 v25, 0xbab8aa3b, v45
	v_mul_f32_e32 v26, 0xbab8aa3b, v46
	v_mul_f32_e32 v27, 0xbab8aa3b, v47
	v_mul_f32_e32 v28, 0xbab8aa3b, v36
	v_mul_f32_e32 v29, 0xbab8aa3b, v37
	v_mul_f32_e32 v30, 0xbab8aa3b, v38
	v_mul_f32_e32 v31, 0xbab8aa3b, v39
	v_min_f32_e32 v24, 0x42200000, v24
	v_min_f32_e32 v25, 0x42200000, v25
	v_min_f32_e32 v26, 0x42200000, v26
	v_min_f32_e32 v27, 0x42200000, v27
	v_min_f32_e32 v28, 0x42200000, v28
	v_min_f32_e32 v29, 0x42200000, v29
	v_min_f32_e32 v30, 0x42200000, v30
	v_min_f32_e32 v31, 0x42200000, v31
	v_exp_f32_e32 v24, v24
	v_exp_f32_e32 v25, v25
	v_exp_f32_e32 v26, v26
	v_exp_f32_e32 v27, v27
	v_exp_f32_e32 v28, v28
	v_exp_f32_e32 v29, v29
	v_exp_f32_e32 v30, v30
	v_exp_f32_e32 v31, v31
	v_mul_f32_e32 v16, v44, v40
	v_mul_f32_e32 v17, v45, v41
	v_mul_f32_e32 v18, v46, v42
	v_mul_f32_e32 v19, v47, v43
	v_mul_f32_e32 v20, v36, v32
	v_mul_f32_e32 v21, v37, v33
	v_mul_f32_e32 v22, v38, v34
	v_mul_f32_e32 v23, v39, v35
	v_fma_f32 v24, v24, s69, s69
	v_fma_f32 v25, v25, s69, s69
	v_fma_f32 v26, v26, s69, s69
	v_fma_f32 v27, v27, s69, s69
	v_fma_f32 v28, v28, s69, s69
	v_fma_f32 v29, v29, s69, s69
	v_fma_f32 v30, v30, s69, s69
	v_fma_f32 v31, v31, s69, s69
	v_mul_f32_e32 v0, v24, v25
	v_mul_f32_e32 v1, v26, v27
	v_mul_f32_e32 v2, v28, v29
	v_mul_f32_e32 v3, v30, v31
	v_rcp_f32_e32 v0, v0
	v_rcp_f32_e32 v1, v1
	v_rcp_f32_e32 v2, v2
	v_rcp_f32_e32 v3, v3
	v_mul_f32_e32 v16, v16, v25
	v_mul_f32_e32 v18, v18, v27
	v_mul_f32_e32 v20, v20, v29
	v_mul_f32_e32 v22, v22, v31
	v_mul_f32_e32 v17, v17, v24
	v_mul_f32_e32 v19, v19, v26
	v_mul_f32_e32 v21, v21, v28
	v_mul_f32_e32 v23, v23, v30
	v_mul_f32_e32 v16, v16, v0
	v_mul_f32_e32 v17, v17, v0
	v_mul_f32_e32 v18, v18, v1
	v_mul_f32_e32 v19, v19, v1
	v_mul_f32_e32 v20, v20, v2
	v_mul_f32_e32 v21, v21, v2
	v_mul_f32_e32 v22, v22, v3
	v_mul_f32_e32 v23, v23, v3
	v_med3_f32 v16, v16, s11, v232
	v_med3_f32 v17, v17, s11, v232
	v_med3_f32 v18, v18, s11, v232
	v_med3_f32 v19, v19, s11, v232
	v_med3_f32 v20, v20, s11, v232
	v_med3_f32 v21, v21, s11, v232
	v_med3_f32 v22, v22, s11, v232
	v_med3_f32 v23, v23, s11, v232
	v_cvt_pk_fp8_f32 v0, v8, v9
	v_cvt_pk_fp8_f32 v1, v12, v13
	v_cvt_pk_fp8_f32 v2, v16, v17
	v_cvt_pk_fp8_f32 v3, v20, v21
	v_cvt_pk_fp8_f32 v0, v10, v11 op_sel:[0,0,1]
	v_cvt_pk_fp8_f32 v1, v14, v15 op_sel:[0,0,1]
	v_cvt_pk_fp8_f32 v2, v18, v19 op_sel:[0,0,1]
	v_cvt_pk_fp8_f32 v3, v22, v23 op_sel:[0,0,1]
	v_add_co_u32_e32 v4, vcc, 0x28000, v4
	s_nop 1
	v_addc_co_u32_e32 v5, vcc, 0, v5, vcc
	s_mov_b64 s[0:1], -1
	s_nop 1
	v_permlane16_swap_b32_e32 v0, v2
	v_permlane16_swap_b32_e32 v1, v3
	s_andn2_b64 vcc, exec, s[38:39]
	global_store_dwordx4 v[4:5], v[0:3], off
	v_mov_b32_e32 v32, 0
	v_mov_b32_e32 v33, 0
	v_mov_b32_e32 v34, 0
	v_mov_b32_e32 v35, 0
	v_mov_b32_e32 v36, 0
	v_mov_b32_e32 v37, 0
	v_mov_b32_e32 v38, 0
	v_mov_b32_e32 v39, 0
	v_mov_b32_e32 v40, 0
	v_mov_b32_e32 v41, 0
	v_mov_b32_e32 v42, 0
	v_mov_b32_e32 v43, 0
	v_mov_b32_e32 v44, 0
	v_mov_b32_e32 v45, 0
	v_mov_b32_e32 v46, 0
	v_mov_b32_e32 v47, 0
	v_mov_b32_e32 v50, 0
	v_mov_b32_e32 v51, 0
	v_mov_b32_e32 v52, 0
	v_mov_b32_e32 v53, 0
	v_mov_b32_e32 v54, 0
	v_mov_b32_e32 v55, 0
	v_mov_b32_e32 v56, 0
	v_mov_b32_e32 v57, 0
	v_mov_b32_e32 v58, 0
	v_mov_b32_e32 v59, 0
	v_mov_b32_e32 v60, 0
	v_mov_b32_e32 v61, 0
	v_mov_b32_e32 v62, 0
	v_mov_b32_e32 v63, 0
	v_mov_b32_e32 v64, 0
	v_mov_b32_e32 v65, 0
	s_cbranch_vccnz .LBB0_849
	s_andn2_b64 vcc, exec, s[56:57]
	s_cbranch_vccnz .LBB0_848
	s_barrier
	s_branch .LBB0_848
